# speedup vs baseline: 1.0897x; 1.0662x over previous
.LBB0_6:
	s_or_b64 exec, exec, s[6:7]
	s_load_dwordx2 s[10:11], s[0:1], 0x30
	v_and_b32_e32 v1, 15, v0
	v_bfe_u32 v2, v0, 4, 2
	v_lshrrev_b32_e32 v3, 6, v0
	s_movk_i32 s8, 0x90
	s_movk_i32 s9, 0x1b0
	v_mul_u32_u24_e32 v4, 0x900, v3
	v_mad_u32_u24 v4, v1, s8, v4
	v_mad_u32_u24 v4, v2, 36, v4
	v_lshlrev_b32_e32 v5, 2, v1
	v_mad_u32_u24 v5, v2, s9, v5
	v_add_u32_e32 v5, 0x2400, v5
	s_waitcnt lgkmcnt(0)
	s_barrier
	ds_read_b32 v10, v4
	ds_read_b32 v11, v4 offset:4
	ds_read_b32 v12, v4 offset:8
	ds_read_b32 v13, v4 offset:12
	ds_read_b32 v14, v4 offset:16
	ds_read_b32 v15, v4 offset:20
	ds_read_b32 v16, v4 offset:24
	ds_read_b32 v17, v4 offset:28
	ds_read_b32 v18, v4 offset:32
	ds_read_b32 v20, v5
	ds_read_b32 v21, v5 offset:72
	ds_read_b32 v22, v5 offset:144
	ds_read_b32 v23, v5 offset:216
	s_waitcnt lgkmcnt(0)
	ds_read_b32 v24, v5 offset:4
	ds_read_b32 v25, v5 offset:76
	ds_read_b32 v26, v5 offset:148
	ds_read_b32 v27, v5 offset:220
	ds_read_b32 v28, v5 offset:8
	ds_read_b32 v29, v5 offset:80
	ds_read_b32 v30, v5 offset:152
	ds_read_b32 v31, v5 offset:224
	v_mfma_f32_16x16x4_f32 v[60:63], v10, v20, 0
	v_mfma_f32_16x16x4_f32 v[64:67], v10, v21, 0
	v_mfma_f32_16x16x4_f32 v[68:71], v10, v22, 0
	v_mfma_f32_16x16x4_f32 v[72:75], v10, v23, 0
	s_waitcnt lgkmcnt(4)
	ds_read_b32 v32, v5 offset:72
	ds_read_b32 v33, v5 offset:144
	ds_read_b32 v34, v5 offset:216
	ds_read_b32 v35, v5 offset:288
	v_mfma_f32_16x16x4_f32 v[60:63], v11, v24, v[60:63]
	v_mfma_f32_16x16x4_f32 v[64:67], v11, v25, v[64:67]
	v_mfma_f32_16x16x4_f32 v[68:71], v11, v26, v[68:71]
	v_mfma_f32_16x16x4_f32 v[72:75], v11, v27, v[72:75]
	s_waitcnt lgkmcnt(4)
	ds_read_b32 v36, v5 offset:76
	ds_read_b32 v37, v5 offset:148
	ds_read_b32 v38, v5 offset:220
	ds_read_b32 v39, v5 offset:292
	v_mfma_f32_16x16x4_f32 v[60:63], v12, v28, v[60:63]
	v_mfma_f32_16x16x4_f32 v[64:67], v12, v29, v[64:67]
	v_mfma_f32_16x16x4_f32 v[68:71], v12, v30, v[68:71]
	v_mfma_f32_16x16x4_f32 v[72:75], v12, v31, v[72:75]
	s_waitcnt lgkmcnt(4)
	ds_read_b32 v40, v5 offset:80
	ds_read_b32 v41, v5 offset:152
	ds_read_b32 v42, v5 offset:224
	ds_read_b32 v43, v5 offset:296
	v_mfma_f32_16x16x4_f32 v[60:63], v13, v32, v[60:63]
	v_mfma_f32_16x16x4_f32 v[64:67], v13, v33, v[64:67]
	v_mfma_f32_16x16x4_f32 v[68:71], v13, v34, v[68:71]
	v_mfma_f32_16x16x4_f32 v[72:75], v13, v35, v[72:75]
	s_waitcnt lgkmcnt(4)
	ds_read_b32 v44, v5 offset:144
	ds_read_b32 v45, v5 offset:216
	ds_read_b32 v46, v5 offset:288
	ds_read_b32 v47, v5 offset:360
	v_mfma_f32_16x16x4_f32 v[60:63], v14, v36, v[60:63]
	v_mfma_f32_16x16x4_f32 v[64:67], v14, v37, v[64:67]
	v_mfma_f32_16x16x4_f32 v[68:71], v14, v38, v[68:71]
	v_mfma_f32_16x16x4_f32 v[72:75], v14, v39, v[72:75]
	s_waitcnt lgkmcnt(4)
	ds_read_b32 v48, v5 offset:148
	ds_read_b32 v49, v5 offset:220
	ds_read_b32 v50, v5 offset:292
	ds_read_b32 v51, v5 offset:364
	v_mfma_f32_16x16x4_f32 v[60:63], v15, v40, v[60:63]
	v_mfma_f32_16x16x4_f32 v[64:67], v15, v41, v[64:67]
	v_mfma_f32_16x16x4_f32 v[68:71], v15, v42, v[68:71]
	v_mfma_f32_16x16x4_f32 v[72:75], v15, v43, v[72:75]
	s_waitcnt lgkmcnt(4)
	ds_read_b32 v52, v5 offset:152
	ds_read_b32 v53, v5 offset:224
	ds_read_b32 v54, v5 offset:296
	ds_read_b32 v55, v5 offset:368
	v_mfma_f32_16x16x4_f32 v[60:63], v16, v44, v[60:63]
	v_mfma_f32_16x16x4_f32 v[64:67], v16, v45, v[64:67]
	v_mfma_f32_16x16x4_f32 v[68:71], v16, v46, v[68:71]
	v_mfma_f32_16x16x4_f32 v[72:75], v16, v47, v[72:75]
	s_waitcnt lgkmcnt(4)
	v_mfma_f32_16x16x4_f32 v[60:63], v17, v48, v[60:63]
	v_mfma_f32_16x16x4_f32 v[64:67], v17, v49, v[64:67]
	v_mfma_f32_16x16x4_f32 v[68:71], v17, v50, v[68:71]
	v_mfma_f32_16x16x4_f32 v[72:75], v17, v51, v[72:75]
	s_waitcnt lgkmcnt(0)
	v_mfma_f32_16x16x4_f32 v[60:63], v18, v52, v[60:63]
	v_mfma_f32_16x16x4_f32 v[64:67], v18, v53, v[64:67]
	v_mfma_f32_16x16x4_f32 v[68:71], v18, v54, v[68:71]
	v_mfma_f32_16x16x4_f32 v[72:75], v18, v55, v[72:75]
	s_lshl_b32 s8, s12, 7
	s_add_i32 s8, s8, s3
	v_add_u32_e32 v6, s8, v1
	v_lshlrev_b32_e32 v6, 7, v6
	v_lshl_add_u32 v6, v3, 5, v6
	v_lshl_add_u32 v6, v2, 3, v6
	v_add_u32_e32 v7, 0x4000, v6
	v_add_u32_e32 v8, 0x8000, v6
	v_add_u32_e32 v9, 0xc000, v6
	v_and_b32_e32 v94, 63, v0
	v_lshlrev_b32_e32 v95, 3, v3
	s_nop 7
	s_nop 7
	v_cvt_pk_f16_f32 v80, v60, v61
	v_cvt_pk_f16_f32 v81, v62, v63
	v_cvt_pk_f16_f32 v82, v64, v65
	v_cvt_pk_f16_f32 v83, v66, v67
	v_cvt_pk_f16_f32 v84, v68, v69
	v_cvt_pk_f16_f32 v85, v70, v71
	v_cvt_pk_f16_f32 v86, v72, v73
	v_cvt_pk_f16_f32 v87, v74, v75
	s_waitcnt lgkmcnt(0)
	global_store_dwordx2 v6, v[80:81], s[10:11]
	global_store_dwordx2 v7, v[82:83], s[10:11]
	global_store_dwordx2 v8, v[84:85], s[10:11]
	global_store_dwordx2 v9, v[86:87], s[10:11]
	v_add_f32_e32 v90, v60, v61
	v_mul_f32_e32 v91, v60, v60
	v_fmac_f32_e32 v91, v61, v61
	v_add_f32_e32 v90, v90, v62
	v_fmac_f32_e32 v91, v62, v62
	v_add_f32_e32 v90, v90, v63
	v_fmac_f32_e32 v91, v63, v63
	v_add_f32_e32 v90, v90, v64
	v_fmac_f32_e32 v91, v64, v64
	v_add_f32_e32 v90, v90, v65
	v_fmac_f32_e32 v91, v65, v65
	v_add_f32_e32 v90, v90, v66
	v_fmac_f32_e32 v91, v66, v66
	v_add_f32_e32 v90, v90, v67
	v_fmac_f32_e32 v91, v67, v67
	v_add_f32_e32 v90, v90, v68
	v_fmac_f32_e32 v91, v68, v68
	v_add_f32_e32 v90, v90, v69
	v_fmac_f32_e32 v91, v69, v69
	v_add_f32_e32 v90, v90, v70
	v_fmac_f32_e32 v91, v70, v70
	v_add_f32_e32 v90, v90, v71
	v_fmac_f32_e32 v91, v71, v71
	v_add_f32_e32 v90, v90, v72
	v_fmac_f32_e32 v91, v72, v72
	v_add_f32_e32 v90, v90, v73
	v_fmac_f32_e32 v91, v73, v73
	v_add_f32_e32 v90, v90, v74
	v_fmac_f32_e32 v91, v74, v74
	v_add_f32_e32 v90, v90, v75
	v_fmac_f32_e32 v91, v75, v75
	v_mov_b32_e32 v96, 0
	v_mov_b32_e32 v97, 0
	v_cmp_eq_u32_e32 vcc, 63, v94
	s_nop 1
	v_mov_b32_dpp v92, v90 row_shr:1 row_mask:0xf bank_mask:0xf bound_ctrl:1
	v_mov_b32_dpp v93, v91 row_shr:1 row_mask:0xf bank_mask:0xf bound_ctrl:1
	v_pk_add_f32 v[90:91], v[90:91], v[92:93]
	s_nop 1
	v_mov_b32_dpp v92, v90 row_shr:2 row_mask:0xf bank_mask:0xf bound_ctrl:1
	v_mov_b32_dpp v93, v91 row_shr:2 row_mask:0xf bank_mask:0xf bound_ctrl:1
	v_pk_add_f32 v[90:91], v[90:91], v[92:93]
	s_nop 1
	v_mov_b32_dpp v92, v90 row_shr:4 row_mask:0xf bank_mask:0xf bound_ctrl:1
	v_mov_b32_dpp v93, v91 row_shr:4 row_mask:0xf bank_mask:0xf bound_ctrl:1
	v_pk_add_f32 v[90:91], v[90:91], v[92:93]
	s_nop 1
	v_mov_b32_dpp v92, v90 row_shr:8 row_mask:0xf bank_mask:0xf bound_ctrl:1
	v_mov_b32_dpp v93, v91 row_shr:8 row_mask:0xf bank_mask:0xf bound_ctrl:1
	v_pk_add_f32 v[90:91], v[90:91], v[92:93]
	v_mov_b32_e32 v92, 0
	v_mov_b32_e32 v93, 0
	s_nop 0
	v_mov_b32_dpp v92, v90 row_bcast:15 row_mask:0xa bank_mask:0xf
	v_mov_b32_dpp v93, v91 row_bcast:15 row_mask:0xa bank_mask:0xf
	v_pk_add_f32 v[90:91], v[90:91], v[92:93]
	s_nop 1
	v_mov_b32_dpp v96, v90 row_bcast:31 row_mask:0xc bank_mask:0xf
	v_mov_b32_dpp v97, v91 row_bcast:31 row_mask:0xc bank_mask:0xf
	s_and_saveexec_b64 s[6:7], vcc
	v_pk_add_f32 v[90:91], v[90:91], v[96:97]
	ds_write_b64 v95, v[90:91] offset:11968
	s_or_b64 exec, exec, s[6:7]
	v_cmp_eq_u32_e32 vcc, 0, v0
	s_waitcnt lgkmcnt(0)
	s_barrier
	s_and_saveexec_b64 s[6:7], vcc
	s_cbranch_execz .LBB0_10
	v_mov_b32_e32 v1, 0
	ds_read_b128 v[2:5], v1 offset:11968
	ds_read_b128 v[6:9], v1 offset:11984
	s_lshl_b32 s8, s2, 1
	s_mov_b32 s9, 0
	s_lshl_b64 s[8:9], s[8:9], 2
	s_waitcnt lgkmcnt(1)
	v_pk_add_f32 v[2:3], v[2:3], v[4:5]
	s_add_u32 s4, s4, s8
	s_waitcnt lgkmcnt(0)
	v_pk_add_f32 v[2:3], v[2:3], v[6:7]
	s_addc_u32 s5, s5, s9
	v_pk_add_f32 v[2:3], v[2:3], v[8:9]
	global_store_dwordx2 v1, v[2:3], s[4:5]

.LBB3_12:
	s_or_b64 exec, exec, s[2:3]
	v_lshlrev_b32_e32 v28, 2, v1
	s_waitcnt lgkmcnt(0)
	global_load_dword v32, v28, s[16:17]
	global_load_dword v31, v28, s[18:19]
	s_movk_i32 s38, 0xff94
	s_movk_i32 s39, 0xffee
	s_add_i32 s40, s22, -4
	v_mov_b32_e32 v131, 0x7f
	v_mov_b32_e32 v132, 0x7c
	v_min_u32_e32 v133, 27, v50
	v_min_u32_e32 v134, 3, v48
	v_or_b32_e32 v134, 24, v134
	v_lshl_or_b32 v128, v48, 6, v1
	v_mul_u32_u24_e32 v129, 0x25f, v128
	v_lshrrev_b32_e32 v129, 16, v129
	v_mad_i32_i24 v128, v129, s38, v128
	v_mul_u32_u24_e32 v130, 0xe39, v128
	v_lshrrev_b32_e32 v130, 16, v130
	v_mad_i32_i24 v128, v130, s39, v128
	v_add_u32_e32 v130, s25, v130
	v_med3_i32 v130, v130, 0, v131
	v_lshl_add_u32 v128, v128, 2, s40
	v_med3_i32 v128, v128, 0, v132
	v_min_u32_e32 v129, 15, v129
	v_lshlrev_b32_e32 v129, 14, v129
	v_lshlrev_b32_e32 v130, 7, v130
	v_or3_b32 v94, v130, v129, v128
	v_lshl_or_b32 v128, v49, 6, v1
	v_mul_u32_u24_e32 v129, 0x25f, v128
	v_lshrrev_b32_e32 v129, 16, v129
	v_mad_i32_i24 v128, v129, s38, v128
	v_mul_u32_u24_e32 v130, 0xe39, v128
	v_lshrrev_b32_e32 v130, 16, v130
	v_mad_i32_i24 v128, v130, s39, v128
	v_add_u32_e32 v130, s25, v130
	v_med3_i32 v130, v130, 0, v131
	v_lshl_add_u32 v128, v128, 2, s40
	v_med3_i32 v128, v128, 0, v132
	v_min_u32_e32 v129, 15, v129
	v_lshlrev_b32_e32 v129, 14, v129
	v_lshlrev_b32_e32 v130, 7, v130
	v_or3_b32 v96, v130, v129, v128
	v_lshl_or_b32 v128, v133, 6, v1
	v_mul_u32_u24_e32 v129, 0x25f, v128
	v_lshrrev_b32_e32 v129, 16, v129
	v_mad_i32_i24 v128, v129, s38, v128
	v_mul_u32_u24_e32 v130, 0xe39, v128
	v_lshrrev_b32_e32 v130, 16, v130
	v_mad_i32_i24 v128, v130, s39, v128
	v_add_u32_e32 v130, s25, v130
	v_med3_i32 v130, v130, 0, v131
	v_lshl_add_u32 v128, v128, 2, s40
	v_med3_i32 v128, v128, 0, v132
	v_min_u32_e32 v129, 15, v129
	v_lshlrev_b32_e32 v129, 14, v129
	v_lshlrev_b32_e32 v130, 7, v130
	v_or3_b32 v98, v130, v129, v128
	v_lshl_or_b32 v128, v134, 6, v1
	v_mul_u32_u24_e32 v129, 0x25f, v128
	v_lshrrev_b32_e32 v129, 16, v129
	v_mad_i32_i24 v128, v129, s38, v128
	v_mul_u32_u24_e32 v130, 0xe39, v128
	v_lshrrev_b32_e32 v130, 16, v130
	v_mad_i32_i24 v128, v130, s39, v128
	v_add_u32_e32 v130, s25, v130
	v_med3_i32 v130, v130, 0, v131
	v_lshl_add_u32 v128, v128, 2, s40
	v_med3_i32 v128, v128, 0, v132
	v_min_u32_e32 v129, 15, v129
	v_lshlrev_b32_e32 v129, 14, v129
	v_lshlrev_b32_e32 v130, 7, v130
	v_or3_b32 v100, v130, v129, v128
	v_accvgpr_write_b32 a3, 0
	v_accvgpr_write_b32 a2, 0
	v_accvgpr_write_b32 a1, 0
	v_accvgpr_write_b32 a0, 0
	v_accvgpr_write_b32 a7, 0
	v_accvgpr_write_b32 a6, 0
	v_accvgpr_write_b32 a5, 0
	v_accvgpr_write_b32 a4, 0
	v_accvgpr_write_b32 a15, 0
	v_accvgpr_write_b32 a14, 0
	v_accvgpr_write_b32 a13, 0
	v_accvgpr_write_b32 a12, 0
	v_accvgpr_write_b32 a19, 0
	v_accvgpr_write_b32 a18, 0
	v_accvgpr_write_b32 a17, 0
	v_accvgpr_write_b32 a16, 0
	v_accvgpr_write_b32 a31, 0
	v_accvgpr_write_b32 a30, 0
	v_accvgpr_write_b32 a29, 0
	v_accvgpr_write_b32 a28, 0
	v_accvgpr_write_b32 a63, 0
	v_accvgpr_write_b32 a62, 0
	v_accvgpr_write_b32 a61, 0
	v_accvgpr_write_b32 a60, 0
	v_accvgpr_write_b32 a11, 0
	v_accvgpr_write_b32 a10, 0
	v_accvgpr_write_b32 a9, 0
	v_accvgpr_write_b32 a8, 0
	v_accvgpr_write_b32 a23, 0
	v_accvgpr_write_b32 a22, 0
	v_accvgpr_write_b32 a21, 0
	v_accvgpr_write_b32 a20, 0
	v_accvgpr_write_b32 a27, 0
	v_accvgpr_write_b32 a26, 0
	v_accvgpr_write_b32 a25, 0
	v_accvgpr_write_b32 a24, 0
	v_accvgpr_write_b32 a39, 0
	v_accvgpr_write_b32 a38, 0
	v_accvgpr_write_b32 a37, 0
	v_accvgpr_write_b32 a36, 0
	v_accvgpr_write_b32 a47, 0
	v_accvgpr_write_b32 a46, 0
	v_accvgpr_write_b32 a45, 0
	v_accvgpr_write_b32 a44, 0
	v_accvgpr_write_b32 a67, 0
	v_accvgpr_write_b32 a66, 0
	v_accvgpr_write_b32 a65, 0
	v_accvgpr_write_b32 a64, 0
	v_accvgpr_write_b32 a35, 0
	v_accvgpr_write_b32 a34, 0
	v_accvgpr_write_b32 a33, 0
	v_accvgpr_write_b32 a32, 0
	v_accvgpr_write_b32 a43, 0
	v_accvgpr_write_b32 a42, 0
	v_accvgpr_write_b32 a41, 0
	v_accvgpr_write_b32 a40, 0
	v_accvgpr_write_b32 a51, 0
	v_accvgpr_write_b32 a50, 0
	v_accvgpr_write_b32 a49, 0
	v_accvgpr_write_b32 a48, 0
	v_accvgpr_write_b32 a55, 0
	v_accvgpr_write_b32 a54, 0
	v_accvgpr_write_b32 a53, 0
	v_accvgpr_write_b32 a52, 0
	v_accvgpr_write_b32 a59, 0
	v_accvgpr_write_b32 a58, 0
	v_accvgpr_write_b32 a57, 0
	v_accvgpr_write_b32 a56, 0
	v_accvgpr_write_b32 a71, 0
	v_accvgpr_write_b32 a70, 0
	v_accvgpr_write_b32 a69, 0
	v_accvgpr_write_b32 a68, 0
	s_waitcnt vmcnt(0)
	v_mov_b32_dpp v28, v26 row_shr:1 row_mask:0xf bank_mask:0xf bound_ctrl:1
	v_mov_b32_dpp v29, v27 row_shr:1 row_mask:0xf bank_mask:0xf bound_ctrl:1
	v_pk_add_f32 v[26:27], v[26:27], v[28:29]
	v_mov_b32_e32 v34, 0
	v_mov_b32_e32 v35, 0
	v_mov_b32_dpp v28, v26 row_shr:2 row_mask:0xf bank_mask:0xf bound_ctrl:1
	v_mov_b32_dpp v29, v27 row_shr:2 row_mask:0xf bank_mask:0xf bound_ctrl:1
	v_pk_add_f32 v[26:27], v[26:27], v[28:29]
	v_cmp_eq_u32_e32 vcc, 63, v1
	s_nop 0
	v_mov_b32_dpp v28, v26 row_shr:4 row_mask:0xf bank_mask:0xf bound_ctrl:1
	v_mov_b32_dpp v29, v27 row_shr:4 row_mask:0xf bank_mask:0xf bound_ctrl:1
	v_pk_add_f32 v[26:27], v[26:27], v[28:29]
	s_nop 1
	v_mov_b32_dpp v28, v26 row_shr:8 row_mask:0xf bank_mask:0xf bound_ctrl:1
	v_mov_b32_dpp v29, v27 row_shr:8 row_mask:0xf bank_mask:0xf bound_ctrl:1
	v_pk_add_f32 v[28:29], v[26:27], v[28:29]
	v_mov_b32_e32 v27, 0
	v_mov_b32_e32 v26, 0
	v_mov_b32_dpp v34, v28 row_bcast:15 row_mask:0xa bank_mask:0xf
	v_mov_b32_dpp v35, v29 row_bcast:15 row_mask:0xa bank_mask:0xf
	v_pk_add_f32 v[28:29], v[28:29], v[34:35]
	s_nop 1
	v_mov_b32_dpp v26, v28 row_bcast:31 row_mask:0xc bank_mask:0xf
	v_mov_b32_dpp v27, v29 row_bcast:31 row_mask:0xc bank_mask:0xf
	s_and_saveexec_b64 s[2:3], vcc
	v_lshl_add_u32 v33, v48, 3, 0
	v_add_u32_e32 v33, 0x15800, v33
	v_pk_add_f32 v[26:27], v[28:29], v[26:27]
	ds_write_b64 v33, v[26:27]
	s_or_b64 exec, exec, s[2:3]
	v_cmp_gt_u32_e32 vcc, 64, v0
	s_waitcnt lgkmcnt(0)
	s_barrier
	s_and_saveexec_b64 s[10:11], vcc
	s_cbranch_execz .LBB3_16
	s_add_i32 s2, 0, 0x15800
	v_mov_b32_e32 v26, s2
	s_add_i32 s2, 0, 0x15810
	v_mov_b32_e32 v33, s2
	ds_read_b128 v[26:29], v26
	ds_read_b128 v[34:37], v33
	s_mov_b32 s2, 0xf800000
	s_waitcnt lgkmcnt(1)
	v_add_f32_e32 v26, v26, v28
	s_waitcnt lgkmcnt(0)
	v_add_f32_e32 v28, v34, v36
	v_add_f32_e32 v26, v26, v28
	v_add_f32_e32 v27, v27, v29
	v_add_f32_e32 v28, v35, v37
	v_add_f32_e32 v27, v27, v28
	v_mul_f32_e32 v26, 0x35800000, v26
	v_mul_f32_e32 v27, 0x35800000, v27
	v_fma_f32 v27, -v26, v26, v27
	v_add_f32_e32 v27, 0x3727c5ac, v27
	v_mul_f32_e32 v28, 0x4f800000, v27
	v_cmp_gt_f32_e32 vcc, s2, v27
	s_nop 1
	v_cndmask_b32_e32 v27, v27, v28, vcc
	v_sqrt_f32_e32 v28, v27
	s_nop 0
	v_add_u32_e32 v29, -1, v28
	v_fma_f32 v33, -v29, v28, v27
	v_cmp_ge_f32_e64 s[2:3], 0, v33
	v_add_u32_e32 v33, 1, v28
	s_nop 0
	v_cndmask_b32_e64 v29, v28, v29, s[2:3]
	v_fma_f32 v28, -v33, v28, v27
	v_cmp_lt_f32_e64 s[2:3], 0, v28
	s_nop 1
	v_cndmask_b32_e64 v28, v29, v33, s[2:3]
	v_mul_f32_e32 v29, 0x37800000, v28
	v_cndmask_b32_e32 v28, v28, v29, vcc
	v_mov_b32_e32 v29, 0x260
	v_cmp_class_f32_e32 vcc, v27, v29
	s_nop 1
	v_cndmask_b32_e32 v27, v28, v27, vcc
	v_div_scale_f32 v28, s[2:3], v27, v27, 1.0
	v_rcp_f32_e32 v29, v28
	s_nop 0
	v_fma_f32 v33, -v28, v29, 1.0
	v_fmac_f32_e32 v29, v33, v29
	v_div_scale_f32 v33, vcc, 1.0, v27, 1.0
	v_mul_f32_e32 v34, v33, v29
	v_fma_f32 v35, -v28, v34, v33
	v_fmac_f32_e32 v34, v35, v29
	v_fma_f32 v28, -v28, v34, v33
	v_div_fmas_f32 v28, v28, v29, v34
	v_div_fixup_f32 v27, v28, v27, 1.0
	v_lshl_add_u32 v28, v0, 2, 0
	v_mul_f32_e32 v27, v32, v27
	v_add_u32_e32 v29, 0x15600, v28
	ds_write_b32 v29, v27
	v_fma_f32 v26, -v26, v27, v31
	v_add_u32_e32 v27, 0x15700, v28
	ds_write_b32 v27, v26

.LBB3_20:
	s_or_b64 exec, exec, s[6:7]
	s_load_dwordx2 s[12:13], s[0:1], 0x30
	v_min_u32_e32 v47, 27, v50
	v_min_u32_e32 v2, 3, v48
	v_or_b32_e32 v56, 24, v2
	v_lshrrev_b32_e32 v122, 4, v1
	v_and_b32_e32 v93, 15, v0
	v_lshrrev_b32_e32 v120, 8, v0
	s_lshl_b32 s18, s24, 18
	v_and_b32_e32 v121, 3, v48
	v_lshl_or_b32 v123, v120, 4, v93
	s_movk_i32 s0, 0x42
	s_cmp_lg_u32 0, -1
	v_mad_u32_u24 v1, v121, s0, v123
	s_cselect_b32 s0, 0, 0
	v_lshlrev_b32_e32 v2, 7, v1
	v_bitop3_b32 v3, v1, v122, 7 bitop3:0x6c
	v_add_u32_e32 v1, 33, v1
	s_add_i32 s1, s0, 0xc600
	v_lshl_or_b32 v126, v3, 4, v2
	v_lshlrev_b32_e32 v2, 7, v1
	v_bitop3_b32 v1, v1, v122, 7 bitop3:0x6c
	v_add_u32_e32 v124, s1, v46
	s_add_i32 s1, s0, 0xca00
	v_lshl_or_b32 v127, v1, 4, v2
	v_add_u32_e32 v1, s1, v46
	s_add_i32 s1, s0, 0xce00
	s_waitcnt vmcnt(0)
	s_waitcnt lgkmcnt(0)
	s_barrier
	ds_read_b128 v[42:45], v124
	ds_read_b128 v[38:41], v1
	v_add_u32_e32 v1, s1, v46
	s_add_i32 s1, s0, 0xd200
	ds_read_b128 v[34:37], v1
	v_add_u32_e32 v1, s1, v46
	s_add_i32 s1, s0, 0xd600
	ds_read_b128 v[30:33], v1
	v_add_u32_e32 v1, s1, v46
	s_add_i32 s1, s0, 0xda00
	ds_read_b128 v[26:29], v1
	v_add_u32_e32 v1, s1, v46
	s_add_i32 s1, s0, 0xde00
	ds_read_b128 v[22:25], v1
	v_add_u32_e32 v1, s1, v46
	s_add_i32 s1, s0, 0xe200
	ds_read_b128 v[10:13], v1
	v_add_u32_e32 v1, s1, v46
	s_add_i32 s1, s0, 0xe600
	ds_read_b128 v[6:9], v1
	v_add_u32_e32 v1, s1, v46
	ds_read_b128 v[2:5], v1
	v_add_u32_e32 v1, s0, v126
	ds_read_b128 v[14:17], v1
	v_add_u32_e32 v1, s0, v127
	s_add_i32 s0, s0, 0xea00
	v_add_u32_e32 v125, s0, v46
	s_lshl_b32 s0, s24, 20
	s_add_u32 s10, s2, s0
	v_mov_b32_e32 v95, 0
	v_lshlrev_b32_e32 v0, 4, v0
	ds_read_b128 v[18:21], v1
	s_addc_u32 s11, s3, 0
	v_lshlrev_b32_e32 v91, 10, v47
	v_and_b32_e32 v0, 0x1c00, v0
	v_mov_b32_e32 v1, v95
	v_mov_b32_e32 v47, 0x28800
	s_add_u32 s0, s10, 0x400000
	v_mad_u64_u32 v[54:55], s[2:3], s24, v47, v[0:1]
	s_addc_u32 s1, s11, 0
	v_lshlrev_b32_e32 v48, 2, v94
	v_mov_b32_e32 v49, v95
	v_lshlrev_b32_e32 v50, 2, v96
	v_mov_b32_e32 v51, v95
	v_lshlrev_b32_e32 v52, 2, v98
	v_mov_b32_e32 v53, v95
	v_or_b32_e32 v54, v54, v46
	v_lshlrev_b32_e32 v46, 2, v100
	v_mov_b32_e32 v47, v95
	s_waitcnt lgkmcnt(0)
	v_lshl_add_u64 v[0:1], s[0:1], 0, v[48:49]
	v_lshl_add_u64 v[106:107], s[0:1], 0, v[50:51]
	v_lshl_add_u64 v[110:111], s[0:1], 0, v[52:53]
	v_lshl_add_u64 v[112:113], s[10:11], 0, v[46:47]
	v_lshl_add_u64 v[114:115], s[0:1], 0, v[46:47]
	v_lshl_add_u64 v[46:47], s[20:21], 0, v[54:55]
	s_mov_b64 s[0:1], 0xd000
	v_lshl_add_u64 v[116:117], v[46:47], 0, s[0:1]
	s_movk_i32 s0, 0xc000
	s_movk_i32 s2, 0xe000
	s_mov_b32 s19, 0
	v_lshl_add_u64 v[102:103], s[10:11], 0, v[48:49]
	v_mov_b32_e32 v97, v95
	v_mov_b32_e32 v99, v95
	v_mov_b32_e32 v101, v95
	v_lshlrev_b32_e32 v119, 10, v56
	v_lshl_add_u64 v[104:105], s[10:11], 0, v[50:51]
	v_lshl_add_u64 v[108:109], s[10:11], 0, v[52:53]
	s_mov_b32 s20, 1
	s_mov_b32 s1, -1
	s_mov_b32 s3, -1
	s_add_i32 s17, 0, 0x16000
	s_add_i32 s16, 0, 0x1d000
	s_mov_b64 s[6:7], 0x4800
	v_readfirstlane_b32 s32, v118
	v_readfirstlane_b32 s33, v90
	v_readfirstlane_b32 s34, v92
	s_nop 3
	s_add_i32 s32, s32, 0xc600
	s_add_i32 s33, s33, 0xc600
	s_add_i32 s34, s34, 0xc600

.LBB3_32:
	v_lshl_add_u32 v0, v120, 5, s22
	v_or_b32_e32 v1, s23, v121
	s_movk_i32 s0, 0x7f
	v_lshl_or_b32 v7, v93, 1, v0
	s_movk_i32 s1, 0x7e
	s_nop 15
	s_nop 15
	v_cmp_eq_u32_e64 s[4:5], s1, v7
	s_nop 7
	v_cmp_gt_u32_e32 vcc, s0, v1
	v_accvgpr_read_b32 v5, a14
	v_cmp_eq_u32_e64 s[0:1], 0, v1
	v_or_b32_e32 v4, v93, v7
	v_cmp_eq_u32_e64 s[2:3], 0, v4
	v_cndmask_b32_e64 v14, v5, 0, s[0:1]
	v_accvgpr_read_b32 v5, a13
	v_cndmask_b32_e64 v22, v5, 0, s[0:1]
	v_accvgpr_read_b32 v5, a12
	v_cndmask_b32_e64 v116, v5, 0, s[0:1]
	v_accvgpr_read_b32 v5, a49
	v_cndmask_b32_e32 v16, 0, v5, vcc
	v_accvgpr_read_b32 v5, a48
	v_cndmask_b32_e32 v28, 0, v5, vcc
	v_accvgpr_read_b32 v5, a30
	v_cndmask_b32_e64 v10, v5, 0, s[0:1]
	v_accvgpr_read_b32 v5, a29
	v_cndmask_b32_e64 v24, v5, 0, s[0:1]
	v_accvgpr_read_b32 v5, a28
	v_cndmask_b32_e64 v42, v5, 0, s[0:1]
	v_accvgpr_read_b32 v5, a57
	v_cndmask_b32_e32 v20, 0, v5, vcc
	v_accvgpr_read_b32 v5, a56
	v_cndmask_b32_e32 v38, 0, v5, vcc
	v_accvgpr_read_b32 v5, a6
	v_cndmask_b32_e64 v15, v5, 0, s[0:1]
	v_accvgpr_read_b32 v5, a5
	v_cndmask_b32_e64 v23, v5, 0, s[0:1]
	v_accvgpr_read_b32 v5, a4
	v_cndmask_b32_e64 v117, v5, 0, s[0:1]
	v_accvgpr_read_b32 v5, a41
	v_cndmask_b32_e32 v17, 0, v5, vcc
	v_accvgpr_read_b32 v5, a40
	v_cndmask_b32_e32 v29, 0, v5, vcc
	v_accvgpr_read_b32 v5, a17
	v_cndmask_b32_e64 v37, v5, 0, s[0:1]
	v_accvgpr_read_b32 v5, a16
	v_cndmask_b32_e64 v47, v5, 0, s[0:1]
	v_accvgpr_read_b32 v5, a52
	v_cndmask_b32_e32 v45, 0, v5, vcc
	v_accvgpr_read_b32 v5, a68
	v_cndmask_b32_e32 v12, 0, v5, vcc
	v_accvgpr_read_b32 v5, a0
	s_or_b64 s[8:9], s[2:3], s[0:1]
	v_cmp_eq_u32_e64 s[6:7], 15, v93
	v_accvgpr_read_b32 v11, a8
	v_cndmask_b32_e64 v112, v5, 0, s[8:9]
	v_accvgpr_read_b32 v4, a67
	v_mov_b32_e32 v5, 0x90
	s_and_b64 s[4:5], s[6:7], s[4:5]
	v_mov_b64_e32 v[40:41], v[16:17]
	v_cndmask_b32_e64 v16, v11, 0, s[2:3]
	v_cndmask_b32_e64 v11, 12, v5, s[6:7]
	v_cndmask_b32_e64 v61, v4, 0, s[4:5]
	v_accvgpr_read_b32 v4, a61
	s_or_b64 s[6:7], s[4:5], s[0:1]
	v_cndmask_b32_e64 v87, v4, 0, s[6:7]
	v_accvgpr_read_b32 v4, a60
	v_cndmask_b32_e64 v86, v4, 0, s[6:7]
	v_accvgpr_read_b32 v4, a65
	v_cndmask_b32_e64 v5, v4, 0, s[4:5]
	v_accvgpr_read_b32 v4, a64
	v_cndmask_b32_e64 v4, v4, 0, s[4:5]
	s_lshl_b32 s14, s18, 2
	v_mov_b64_e32 v[32:33], v[4:5]
	v_lshl_or_b32 v4, v122, 18, s14
	v_mov_b32_e32 v5, 0
	v_mov_b64_e32 v[62:63], v[14:15]
	v_lshl_add_u64 v[14:15], s[12:13], 0, v[4:5]
	v_lshlrev_b32_e32 v4, 7, v1
	v_lshl_add_u64 v[14:15], v[4:5], 2, v[14:15]
	v_lshlrev_b32_e32 v4, 2, v7
	v_mul_u32_u24_e32 v1, 24, v122
	v_lshl_add_u64 v[54:55], v[14:15], 0, v[4:5]
	v_mbcnt_lo_u32_b32 v138, -1, 0
	v_mbcnt_hi_u32_b32 v138, -1, v138
	v_and_b32_e32 v138, 1, v138
	v_mul_u32_u24_e32 v138, 0xfff8, v138
	v_add_u32_e32 v138, 0xffff0000, v138
	v_mov_b32_e32 v139, -1
	v_lshl_add_u64 v[134:135], v[54:55], 0, v[138:139]
	s_mov_b32 s28, 0x55555555
	s_mov_b32 s29, 0x55555555
	s_mov_b32 s30, 0xaaaaaaaa
	s_mov_b32 s31, 0xaaaaaaaa
	v_or_b32_e32 v1, v1, v121
	v_lshlrev_b32_e32 v4, 7, v120
	s_movk_i32 s12, 0x120
	v_mad_u32_u24 v1, v1, s12, v4
	s_add_u32 s12, s10, 0x800000
	v_accvgpr_read_b32 v7, a72
	v_mov_b64_e32 v[80:81], v[28:29]
	s_addc_u32 s13, s11, 0
	v_lshlrev_b64 v[28:29], 2, v[94:95]
	v_readfirstlane_b32 s14, v7
	v_add_u32_e32 v7, 0, v90
	v_lshl_add_u64 v[4:5], s[12:13], 0, v[28:29]
	s_mov_b32 m0, s14
	v_lshlrev_b64 v[30:31], 2, v[96:97]
	v_readfirstlane_b32 s14, v7
	v_mov_b32_e32 v14, v7
	v_add_u32_e32 v7, 0, v91
	s_waitcnt lgkmcnt(0)
	s_barrier
	global_load_lds_dwordx4 v[4:5], off nt
	v_lshl_add_u64 v[4:5], s[12:13], 0, v[30:31]
	s_mov_b32 m0, s14
	v_lshlrev_b64 v[56:57], 2, v[98:99]
	v_readfirstlane_b32 s14, v7
	global_load_lds_dwordx4 v[4:5], off nt
	v_lshl_add_u64 v[4:5], s[12:13], 0, v[56:57]
	v_mov_b32_e32 v19, v7
	s_mov_b32 m0, s14
	v_lshlrev_b64 v[58:59], 2, v[100:101]
	v_add_u32_e32 v7, 0, v119
	v_accvgpr_read_b32 v25, a72
	global_load_lds_dwordx4 v[4:5], off nt
	v_lshl_add_u64 v[4:5], s[12:13], 0, v[58:59]
	v_readfirstlane_b32 s12, v7
	v_mov_b32_e32 v21, v7
	s_mov_b32 m0, s12
	s_add_u32 s12, s10, 0xc00000
	v_add_u32_e32 v7, 0x7000, v25
	s_addc_u32 s13, s11, 0
	v_readfirstlane_b32 s14, v7
	v_add_u32_e32 v7, 0x7000, v14
	global_load_lds_dwordx4 v[4:5], off nt
	v_lshl_add_u64 v[4:5], s[12:13], 0, v[28:29]
	s_mov_b32 m0, s14
	v_readfirstlane_b32 s14, v7
	v_add_u32_e32 v7, 0x7000, v19
	global_load_lds_dwordx4 v[4:5], off nt
	v_lshl_add_u64 v[4:5], s[12:13], 0, v[30:31]
	s_mov_b32 m0, s14
	v_readfirstlane_b32 s14, v7
	global_load_lds_dwordx4 v[4:5], off nt
	v_lshl_add_u64 v[4:5], s[12:13], 0, v[56:57]
	s_mov_b32 m0, s14
	v_add_u32_e32 v7, 0x7000, v21
	global_load_lds_dwordx4 v[4:5], off nt
	v_lshl_add_u64 v[4:5], s[12:13], 0, v[58:59]
	v_readfirstlane_b32 s12, v7
	s_mov_b32 m0, s12
	s_add_u32 s12, s10, 0x1000000
	v_add_u32_e32 v7, 0xe000, v25
	s_addc_u32 s13, s11, 0
	v_readfirstlane_b32 s14, v7
	v_add_u32_e32 v7, 0xe000, v14
	global_load_lds_dwordx4 v[4:5], off nt
	v_lshl_add_u64 v[4:5], s[12:13], 0, v[28:29]
	s_mov_b32 m0, s14
	v_readfirstlane_b32 s14, v7
	v_add_u32_e32 v7, 0xe000, v19
	global_load_lds_dwordx4 v[4:5], off nt
	v_lshl_add_u64 v[4:5], s[12:13], 0, v[30:31]
	s_mov_b32 m0, s14
	v_readfirstlane_b32 s14, v7
	global_load_lds_dwordx4 v[4:5], off nt
	v_lshl_add_u64 v[4:5], s[12:13], 0, v[56:57]
	s_mov_b32 m0, s14
	v_add_u32_e32 v7, 0xe000, v21
	global_load_lds_dwordx4 v[4:5], off nt
	v_lshl_add_u64 v[4:5], s[12:13], 0, v[58:59]
	v_readfirstlane_b32 s12, v7
	s_mov_b32 m0, s12
	v_lshl_add_u32 v15, v93, 3, v1
	global_load_lds_dwordx4 v[4:5], off nt
	v_add_u32_e32 v1, v1, v11
	s_waitcnt vmcnt(16)
	v_accvgpr_write_b32 a12, v14
	v_mov_b64_e32 v[124:125], v[56:57]
	v_accvgpr_write_b32 a13, v19
	v_mov_b64_e32 v[126:127], v[58:59]
	v_accvgpr_write_b32 a16, v21
	s_waitcnt lgkmcnt(0)
	s_barrier
	v_add_u32_e32 v14, 0x16010, v15
	v_mov_b32_e32 v122, v15
	v_add_u32_e32 v15, 0x16000, v1
	ds_read_b64 v[64:65], v14
	ds_read_b64 v[66:67], v14 offset:288
	ds_read_b64 v[68:69], v14 offset:576
	ds_read_b64 v[76:77], v14 offset:1728
	ds_read_b64 v[78:79], v14 offset:2016
	ds_read_b64 v[4:5], v14 offset:2304
	ds_read_b64 v[84:85], v14 offset:3456
	ds_read_b64 v[74:75], v14 offset:3744
	ds_read_b64 v[88:89], v14 offset:4032
	ds_read_b64 v[100:101], v14 offset:5184
	ds_read_b64 v[106:107], v14 offset:5472
	ds_read_b64 v[120:121], v14 offset:5760
	ds_read_b32 v43, v15
	ds_read_b32 v19, v15 offset:288
	ds_read_b32 v39, v15 offset:576
	ds_read_b32 v25, v15 offset:1728
	ds_read_b32 v7, v15 offset:2016
	ds_read_b32 v21, v15 offset:2304
	ds_read_b32 v11, v15 offset:3456
	ds_read_b32 v35, v15 offset:3744
	ds_read_b32 v59, v15 offset:4032
	ds_read_b32 v57, v15 offset:5184
	ds_read_b32 v51, v15 offset:5472
	ds_read_b32 v49, v15 offset:5760
	s_waitcnt lgkmcnt(0)
	v_accvgpr_read_b32 v8, a26
	v_mov_b32_e32 v46, v43
	v_mov_b32_e32 v113, v65
	v_mov_b32_e32 v26, v19
	v_mov_b32_dpp v46, v65 row_shr:1 row_mask:0xf bank_mask:0xf
	v_pk_mul_f32 v[70:71], v[112:113], v[46:47]
	v_accvgpr_read_b32 v9, a22
	v_accvgpr_read_b32 v27, a36
	v_mov_b32_dpp v43, v64 row_shl:1 row_mask:0xf bank_mask:0xf
	v_mov_b32_dpp v26, v67 row_shr:1 row_mask:0xf bank_mask:0xf
	v_pk_fma_f32 v[70:71], v[64:65], v[116:117], v[70:71] op_sel_hi:[0,1,1]
	v_pk_mov_b32 v[64:65], v[64:65], v[86:87] op_sel:[1,0]
	v_mov_b32_e32 v17, v67
	v_mov_b64_e32 v[102:103], v[8:9]
	v_accvgpr_read_b32 v8, a25
	v_accvgpr_read_b32 v114, a24
	v_accvgpr_read_b32 v9, a21
	v_accvgpr_read_b32 v115, a20
	v_accvgpr_read_b32 v2, a32
	v_mov_b64_e32 v[82:83], v[30:31]
	v_pk_fma_f32 v[70:71], v[64:65], v[42:43], v[70:71]
	v_pk_mul_f32 v[64:65], v[16:17], v[26:27]
	v_mov_b64_e32 v[30:31], v[32:33]
	v_accvgpr_read_b32 v18, a44
	v_mov_b64_e32 v[104:105], v[8:9]
	v_cndmask_b32_e32 v9, 0, v2, vcc
	v_accvgpr_write_b32 a4, v14
	v_mov_b32_dpp v19, v66 row_shl:1 row_mask:0xf bank_mask:0xf
	v_pk_fma_f32 v[64:65], v[66:67], v[114:115], v[64:65] op_sel_hi:[0,1,1]
	v_pk_mov_b32 v[66:67], v[66:67], v[30:31] op_sel:[1,0]
	v_accvgpr_read_b32 v14, a69
	v_mov_b32_e32 v44, v39
	v_mov_b32_e32 v60, v1
	v_pk_fma_f32 v[66:67], v[66:67], v[18:19], v[64:65]
	v_cndmask_b32_e32 v14, 0, v14, vcc
	v_cndmask_b32_e64 v0, v9, 0, s[2:3]
	v_mov_b32_dpp v44, v69 row_shr:1 row_mask:0xf bank_mask:0xf
	v_pk_add_f32 v[70:71], v[70:71], 0 op_sel_hi:[1,0]
	v_mov_b32_e32 v1, v69
	v_accvgpr_write_b32 a0, v15
	v_cndmask_b32_e64 v15, v14, 0, s[4:5]
	v_cndmask_b32_e64 v14, v12, 0, s[4:5]
	v_pk_add_f32 v[66:67], v[70:71], v[66:67]
	v_pk_mul_f32 v[70:71], v[0:1], v[44:45]
	v_mov_b32_dpp v39, v68 row_shl:1 row_mask:0xf bank_mask:0xf
	v_pk_fma_f32 v[70:71], v[68:69], v[80:81], v[70:71] op_sel_hi:[0,1,1]
	v_pk_mov_b32 v[68:69], v[68:69], v[14:15] op_sel:[1,0]
	v_accvgpr_read_b32 v9, a1
	v_pk_fma_f32 v[68:69], v[68:69], v[38:39], v[70:71]
	v_mov_b32_e32 v36, v25
	v_cndmask_b32_e64 v64, v9, 0, s[8:9]
	v_pk_add_f32 v[66:67], v[66:67], v[68:69]
	v_mov_b32_dpp v36, v77 row_shr:1 row_mask:0xf bank_mask:0xf
	v_mov_b32_e32 v65, v77
	v_mov_b64_e32 v[108:109], v[22:23]
	v_accvgpr_read_b32 v9, a9
	v_mov_b32_e32 v128, v66
	v_mov_b32_e32 v129, v67
	v_mov_b32_e32 v12, v7
	v_pk_mul_f32 v[66:67], v[64:65], v[36:37]
	v_accvgpr_read_b32 v13, a37
	v_mov_b64_e32 v[72:73], v[28:29]
	v_cndmask_b32_e64 v28, v9, 0, s[2:3]
	v_mov_b32_dpp v25, v76 row_shl:1 row_mask:0xf bank_mask:0xf
	v_mov_b32_dpp v12, v79 row_shr:1 row_mask:0xf bank_mask:0xf
	v_pk_fma_f32 v[66:67], v[76:77], v[108:109], v[66:67] op_sel_hi:[0,1,1]
	v_mov_b32_e32 v76, v77
	v_mov_b32_e32 v77, v87
	v_mov_b32_e32 v29, v79
	v_pk_fma_f32 v[66:67], v[76:77], v[24:25], v[66:67]
	v_pk_mul_f32 v[76:77], v[28:29], v[12:13]
	v_accvgpr_read_b32 v6, a45
	v_accvgpr_read_b32 v2, a33
	v_mov_b32_dpp v7, v78 row_shl:1 row_mask:0xf bank_mask:0xf
	v_pk_fma_f32 v[76:77], v[78:79], v[104:105], v[76:77] op_sel_hi:[0,1,1]
	v_mov_b32_e32 v78, v79
	v_mov_b32_e32 v79, v31
	v_cndmask_b32_e32 v2, 0, v2, vcc
	v_accvgpr_read_b32 v50, a53
	v_pk_fma_f32 v[76:77], v[78:79], v[6:7], v[76:77]
	v_mov_b32_e32 v78, v21
	v_accvgpr_write_b32 a44, v80
	v_cndmask_b32_e32 v79, 0, v50, vcc
	v_cndmask_b32_e64 v52, v2, 0, s[2:3]
	v_mov_b32_dpp v78, v5 row_shr:1 row_mask:0xf bank_mask:0xf
	v_pk_add_f32 v[66:67], v[66:67], 0 op_sel_hi:[1,0]
	v_mov_b32_e32 v53, v5
	v_accvgpr_write_b32 a45, v81
	v_accvgpr_write_b32 a21, v15
	v_pk_add_f32 v[80:81], v[66:67], v[76:77]
	v_pk_mul_f32 v[66:67], v[52:53], v[78:79]
	v_accvgpr_write_b32 a24, v40
	v_accvgpr_read_b32 v2, a2
	v_mov_b32_dpp v21, v4 row_shl:1 row_mask:0xf bank_mask:0xf
	v_pk_fma_f32 v[66:67], v[4:5], v[40:41], v[66:67] op_sel_hi:[0,1,1]
	v_accvgpr_write_b32 a25, v41
	v_mov_b32_e32 v4, v5
	v_accvgpr_read_b32 v5, a21
	v_cndmask_b32_e64 v40, v2, 0, s[8:9]
	v_accvgpr_read_b32 v2, a62
	v_accvgpr_read_b32 v8, a18
	v_accvgpr_read_b32 v48, a63
	v_accvgpr_write_b32 a20, v14
	v_accvgpr_write_b32 a41, v23
	v_pk_fma_f32 v[4:5], v[4:5], v[20:21], v[66:67]
	s_mov_b64 s[12:13], 0x10000
	v_cndmask_b32_e64 v14, v2, 0, s[6:7]
	v_mov_b32_e32 v76, v11
	v_accvgpr_read_b32 v2, a10
	v_accvgpr_write_b32 a40, v22
	v_cndmask_b32_e64 v15, v48, 0, s[6:7]
	v_cndmask_b32_e64 v77, v8, 0, s[0:1]
	v_pk_add_f32 v[4:5], v[80:81], v[4:5]
	v_lshl_add_u64 v[136:137], v[134:135], 0, s[12:13]
	v_mov_b32_dpp v76, v85 row_shr:1 row_mask:0xf bank_mask:0xf
	v_mov_b32_e32 v41, v85
	v_cndmask_b32_e64 v22, v2, 0, s[2:3]
	v_mov_b32_e32 v2, v35
	v_accvgpr_read_b32 v1, a50
	v_accvgpr_read_b32 v3, a38
	s_mov_b64 s[32:33], vcc
	s_nop 1
	s_mov_b64 vcc, s[28:29]
	s_nop 0
	v_cndmask_b32_dpp v130, v4, v128, vcc quad_perm:[1,0,3,2] row_mask:0xf bank_mask:0xf
	v_cndmask_b32_dpp v131, v5, v129, vcc quad_perm:[1,0,3,2] row_mask:0xf bank_mask:0xf
	s_mov_b64 vcc, s[30:31]
	s_nop 0
	v_cndmask_b32_dpp v132, v128, v4, vcc quad_perm:[1,0,3,2] row_mask:0xf bank_mask:0xf
	v_cndmask_b32_dpp v133, v129, v5, vcc quad_perm:[1,0,3,2] row_mask:0xf bank_mask:0xf
	global_store_dwordx4 v[136:137], v[130:133], off sc0 sc1 nt
	s_nop 1
	s_mov_b64 vcc, s[32:33]
	v_mov_b64_e32 v[8:9], v[14:15]
	v_pk_mul_f32 v[4:5], v[40:41], v[76:77]
	v_mov_b64_e32 v[66:67], v[62:63]
	v_mov_b32_dpp v2, v75 row_shr:1 row_mask:0xf bank_mask:0xf
	v_mov_b32_e32 v23, v75
	v_cndmask_b32_e32 v62, 0, v1, vcc
	v_accvgpr_read_b32 v1, a42
	v_mov_b32_dpp v11, v84 row_shl:1 row_mask:0xf bank_mask:0xf
	v_pk_fma_f32 v[4:5], v[84:85], v[66:67], v[4:5] op_sel_hi:[0,1,1]
	v_pk_mov_b32 v[80:81], v[84:85], v[8:9] op_sel:[1,0]
	v_pk_mul_f32 v[84:85], v[22:23], v[2:3]
	v_accvgpr_read_b32 v2, a58
	v_cndmask_b32_e32 v63, 0, v1, vcc
	v_accvgpr_read_b32 v1, a70
	v_pk_fma_f32 v[80:81], v[80:81], v[10:11], v[4:5]
	v_accvgpr_read_b32 v4, a66
	v_cndmask_b32_e32 v58, 0, v2, vcc
	v_cndmask_b32_e32 v1, 0, v1, vcc
	v_accvgpr_read_b32 v2, a71
	v_cndmask_b32_e64 v8, v4, 0, s[4:5]
	v_cndmask_b32_e32 v2, 0, v2, vcc
	v_cndmask_b32_e64 v4, v1, 0, s[4:5]
	v_accvgpr_read_b32 v1, a34
	v_mov_b32_e32 v9, v61
	v_cndmask_b32_e64 v5, v2, 0, s[4:5]
	v_cndmask_b32_e32 v1, 0, v1, vcc
	v_accvgpr_read_b32 v2, a54
	v_mov_b32_e32 v92, v59
	v_accvgpr_read_b32 v34, a46
	v_mov_b32_dpp v35, v74 row_shl:1 row_mask:0xf bank_mask:0xf
	v_pk_fma_f32 v[84:85], v[74:75], v[102:103], v[84:85] op_sel_hi:[0,1,1]
	v_pk_mov_b32 v[74:75], v[74:75], v[8:9] op_sel:[1,0]
	v_cndmask_b32_e32 v93, 0, v2, vcc
	v_mov_b32_dpp v92, v89 row_shr:1 row_mask:0xf bank_mask:0xf
	v_cndmask_b32_e64 v96, v1, 0, s[2:3]
	v_mov_b32_e32 v97, v89
	v_accvgpr_read_b32 v1, a31
	v_pk_fma_f32 v[74:75], v[74:75], v[34:35], v[84:85]
	v_pk_mul_f32 v[84:85], v[96:97], v[92:93]
	v_accvgpr_write_b32 a8, v62
	v_cndmask_b32_e64 v56, v1, 0, s[0:1]
	v_accvgpr_read_b32 v1, a15
	v_pk_fma_f32 v[84:85], v[88:89], v[62:63], v[84:85] op_sel_hi:[0,1,1]
	v_accvgpr_write_b32 a9, v63
	v_cndmask_b32_e64 v62, v1, 0, s[0:1]
	v_accvgpr_read_b32 v1, a7
	v_cndmask_b32_e64 v63, v1, 0, s[0:1]
	v_accvgpr_read_b32 v1, a19
	v_pk_add_f32 v[80:81], v[80:81], 0 op_sel_hi:[1,0]
	v_mov_b32_dpp v59, v88 row_shl:1 row_mask:0xf bank_mask:0xf
	v_pk_mov_b32 v[88:89], v[88:89], v[4:5] op_sel:[1,0]
	v_cndmask_b32_e64 v95, v1, 0, s[0:1]
	v_accvgpr_read_b32 v1, a3
	v_accvgpr_write_b32 a36, v104
	v_pk_add_f32 v[80:81], v[80:81], v[74:75]
	v_pk_fma_f32 v[84:85], v[88:89], v[58:59], v[84:85]
	v_mov_b32_e32 v94, v57
	v_cndmask_b32_e64 v98, v1, 0, s[8:9]
	v_accvgpr_read_b32 v1, a11
	v_accvgpr_write_b32 a37, v105
	v_accvgpr_write_b32 a32, v102
	v_pk_add_f32 v[80:81], v[80:81], v[84:85]
	s_mov_b64 s[4:5], 0x20000
	v_mov_b32_dpp v94, v101 row_shr:1 row_mask:0xf bank_mask:0xf
	v_mov_b32_e32 v99, v101
	v_cndmask_b32_e64 v104, v1, 0, s[2:3]
	v_accvgpr_read_b32 v1, a59
	v_accvgpr_write_b32 a29, v15
	v_accvgpr_write_b32 a33, v103
	v_accvgpr_write_b32 a49, v5
	v_lshl_add_u64 v[84:85], v[54:55], 0, s[4:5]
	v_mov_b32_e32 v128, v80
	v_mov_b32_e32 v129, v81
	v_pk_mul_f32 v[80:81], v[98:99], v[94:95]
	v_mov_b32_e32 v102, v51
	v_cndmask_b32_e32 v48, 0, v1, vcc
	v_accvgpr_read_b32 v1, a51
	v_accvgpr_write_b32 a48, v4
	v_mov_b32_dpp v57, v100 row_shl:1 row_mask:0xf bank_mask:0xf
	v_pk_fma_f32 v[80:81], v[100:101], v[62:63], v[80:81] op_sel_hi:[0,1,1]
	v_mov_b32_e32 v84, v101
	v_accvgpr_read_b32 v85, a29
	v_accvgpr_read_b32 v103, a39
	v_mov_b32_dpp v102, v107 row_shr:1 row_mask:0xf bank_mask:0xf
	v_mov_b32_e32 v105, v107
	v_cndmask_b32_e32 v4, 0, v1, vcc
	v_accvgpr_read_b32 v1, a43
	v_pk_fma_f32 v[80:81], v[84:85], v[56:57], v[80:81]
	v_accvgpr_read_b32 v30, a27
	v_accvgpr_read_b32 v31, a23
	v_pk_mul_f32 v[84:85], v[104:105], v[102:103]
	v_cndmask_b32_e32 v5, 0, v1, vcc
	v_accvgpr_read_b32 v1, a35
	v_accvgpr_read_b32 v50, a47
	v_mov_b32_dpp v51, v106 row_shl:1 row_mask:0xf bank_mask:0xf
	v_pk_fma_f32 v[84:85], v[106:107], v[30:31], v[84:85] op_sel_hi:[0,1,1]
	v_mov_b32_e32 v106, v107
	v_mov_b32_e32 v107, v9
	v_cndmask_b32_e32 v1, 0, v1, vcc
	v_accvgpr_read_b32 v2, a55
	v_mov_b32_e32 v108, v49
	v_pk_fma_f32 v[84:85], v[106:107], v[50:51], v[84:85]
	v_pk_add_f32 v[80:81], v[80:81], 0 op_sel_hi:[1,0]
	v_cndmask_b32_e32 v109, 0, v2, vcc
	v_mov_b32_dpp v108, v121 row_shr:1 row_mask:0xf bank_mask:0xf
	v_cndmask_b32_e64 v110, v1, 0, s[2:3]
	v_mov_b32_e32 v111, v121
	v_pk_add_f32 v[80:81], v[80:81], v[84:85]
	v_pk_mul_f32 v[84:85], v[110:111], v[108:109]
	v_mov_b32_dpp v49, v120 row_shl:1 row_mask:0xf bank_mask:0xf
	v_pk_fma_f32 v[84:85], v[120:121], v[4:5], v[84:85] op_sel_hi:[0,1,1]
	v_mov_b32_e32 v120, v121
	v_accvgpr_read_b32 v121, a49
	v_pk_fma_f32 v[84:85], v[120:121], v[48:49], v[84:85]
	s_mov_b64 s[0:1], 0x30000
	v_pk_add_f32 v[80:81], v[80:81], v[84:85]
	v_lshl_add_u64 v[136:137], v[134:135], 0, s[0:1]
	v_add_u32_e32 v1, s17, v118
	s_add_u32 s0, s10, 0x1400000
	s_mov_b64 s[32:33], vcc
	s_nop 1
	s_mov_b64 vcc, s[28:29]
	s_nop 0
	v_cndmask_b32_dpp v130, v80, v128, vcc quad_perm:[1,0,3,2] row_mask:0xf bank_mask:0xf
	v_cndmask_b32_dpp v131, v81, v129, vcc quad_perm:[1,0,3,2] row_mask:0xf bank_mask:0xf
	s_mov_b64 vcc, s[30:31]
	s_nop 0
	v_cndmask_b32_dpp v132, v128, v80, vcc quad_perm:[1,0,3,2] row_mask:0xf bank_mask:0xf
	v_cndmask_b32_dpp v133, v129, v81, vcc quad_perm:[1,0,3,2] row_mask:0xf bank_mask:0xf
	global_store_dwordx4 v[136:137], v[130:133], off sc0 sc1 nt
	s_nop 1
	s_mov_b64 vcc, s[32:33]
	v_readfirstlane_b32 s2, v1
	s_addc_u32 s1, s11, 0
	v_add_u32_e32 v1, s17, v90
	s_waitcnt vmcnt(14)
	v_lshl_add_u64 v[80:81], s[0:1], 0, v[72:73]
	s_mov_b32 m0, s2
	v_readfirstlane_b32 s2, v1
	v_mov_b64_e32 v[74:75], v[82:83]
	v_add_u32_e32 v1, s17, v91
	s_waitcnt lgkmcnt(0)
	s_barrier
	global_load_lds_dwordx4 v[80:81], off nt
	v_lshl_add_u64 v[80:81], s[0:1], 0, v[74:75]
	s_mov_b32 m0, s2
	v_readfirstlane_b32 s2, v1
	v_add_u32_e32 v1, s17, v119
	global_load_lds_dwordx4 v[80:81], off nt
	v_lshl_add_u64 v[80:81], s[0:1], 0, v[124:125]
	s_mov_b32 m0, s2
	v_readfirstlane_b32 s2, v1
	global_load_lds_dwordx4 v[80:81], off nt
	v_lshl_add_u64 v[80:81], s[0:1], 0, v[126:127]
	s_mov_b32 m0, s2
	v_accvgpr_write_b32 a53, v33
	v_accvgpr_write_b32 a2, v62
	v_accvgpr_write_b32 a7, v5
	v_accvgpr_write_b32 a22, v124
	v_accvgpr_write_b32 a30, v126
	global_load_lds_dwordx4 v[80:81], off nt
	v_accvgpr_write_b32 a52, v32
	v_accvgpr_write_b32 a3, v63
	v_accvgpr_write_b32 a6, v4
	v_mov_b64_e32 v[32:33], v[72:73]
	v_accvgpr_write_b32 a23, v125
	v_accvgpr_write_b32 a31, v127
	v_add_u32_e32 v2, 0x1d010, v122
	v_accvgpr_write_b32 a10, v122
	v_add_u32_e32 v5, 0x1d000, v60
	v_mov_b32_e32 v4, v60
	ds_read_b64 v[62:63], v2
	ds_read_b64 v[60:61], v2 offset:288
	ds_read_b64 v[72:73], v2 offset:576
	ds_read_b64 v[70:71], v2 offset:1728
	ds_read_b64 v[68:69], v2 offset:2016
	ds_read_b64 v[82:83], v2 offset:2304
	ds_read_b64 v[80:81], v2 offset:3456
	ds_read_b64 v[84:85], v2 offset:3744
	ds_read_b64 v[126:127], v2 offset:4032
	ds_read_b64 v[124:125], v2 offset:5184
	ds_read_b64 v[122:123], v2 offset:5472
	ds_read_b64 v[120:121], v2 offset:5760
	ds_read_b32 v43, v5
	ds_read_b32 v19, v5 offset:288
	ds_read_b32 v39, v5 offset:576
	ds_read_b32 v25, v5 offset:1728
	ds_read_b32 v7, v5 offset:2016
	ds_read_b32 v21, v5 offset:2304
	ds_read_b32 v11, v5 offset:3456
	ds_read_b32 v35, v5 offset:3744
	ds_read_b32 v59, v5 offset:4032
	ds_read_b32 v57, v5 offset:5184
	ds_read_b32 v51, v5 offset:5472
	ds_read_b32 v49, v5 offset:5760
	s_waitcnt lgkmcnt(0)
	v_mov_b64_e32 v[100:101], v[86:87]
	v_mov_b32_e32 v46, v43
	v_mov_b32_e32 v113, v63
	v_mov_b32_e32 v26, v19
	v_mov_b32_dpp v46, v63 row_shr:1 row_mask:0xf bank_mask:0xf
	v_pk_mul_f32 v[88:89], v[112:113], v[46:47]
	v_mov_b32_dpp v43, v62 row_shl:1 row_mask:0xf bank_mask:0xf
	v_pk_fma_f32 v[88:89], v[62:63], v[116:117], v[88:89] op_sel_hi:[0,1,1]
	v_pk_mov_b32 v[62:63], v[62:63], v[100:101] op_sel:[1,0]
	v_mov_b32_dpp v26, v61 row_shr:1 row_mask:0xf bank_mask:0xf
	v_mov_b32_e32 v17, v61
	v_pk_fma_f32 v[62:63], v[62:63], v[42:43], v[88:89]
	v_pk_mul_f32 v[88:89], v[16:17], v[26:27]
	v_accvgpr_write_b32 a34, v16
	v_accvgpr_read_b32 v16, a52
	v_accvgpr_read_b32 v17, a53
	v_mov_b32_dpp v19, v60 row_shl:1 row_mask:0xf bank_mask:0xf
	v_pk_fma_f32 v[88:89], v[60:61], v[114:115], v[88:89] op_sel_hi:[0,1,1]
	v_pk_mov_b32 v[60:61], v[60:61], v[16:17] op_sel:[1,0]
	v_mov_b32_e32 v44, v39
	v_accvgpr_write_b32 a28, v14
	v_pk_fma_f32 v[60:61], v[60:61], v[18:19], v[88:89]
	v_pk_add_f32 v[62:63], v[62:63], 0 op_sel_hi:[1,0]
	v_mov_b32_dpp v44, v73 row_shr:1 row_mask:0xf bank_mask:0xf
	v_mov_b32_e32 v1, v73
	v_accvgpr_read_b32 v14, a44
	v_accvgpr_read_b32 v89, a21
	v_pk_add_f32 v[60:61], v[62:63], v[60:61]
	v_pk_mul_f32 v[62:63], v[0:1], v[44:45]
	v_accvgpr_read_b32 v15, a45
	v_accvgpr_read_b32 v88, a20
	v_mov_b32_dpp v39, v72 row_shl:1 row_mask:0xf bank_mask:0xf
	v_pk_fma_f32 v[62:63], v[72:73], v[14:15], v[62:63] op_sel_hi:[0,1,1]
	v_pk_mov_b32 v[72:73], v[72:73], v[88:89] op_sel:[1,0]
	v_mov_b32_e32 v36, v25
	v_pk_fma_f32 v[62:63], v[72:73], v[38:39], v[62:63]
	s_mov_b64 s[0:1], 0x400000
	v_pk_add_f32 v[60:61], v[60:61], v[62:63]
	v_mov_b32_dpp v36, v71 row_shr:1 row_mask:0xf bank_mask:0xf
	v_mov_b32_e32 v65, v71
	v_accvgpr_read_b32 v87, a41
	v_lshl_add_u64 v[62:63], v[54:55], 0, s[0:1]
	v_mov_b32_e32 v128, v60
	v_mov_b32_e32 v129, v61
	v_pk_mul_f32 v[60:61], v[64:65], v[36:37]
	v_accvgpr_read_b32 v86, a40
	v_mov_b32_e32 v12, v7
	v_mov_b32_dpp v25, v70 row_shl:1 row_mask:0xf bank_mask:0xf
	v_pk_fma_f32 v[60:61], v[70:71], v[86:87], v[60:61] op_sel_hi:[0,1,1]
	v_mov_b32_e32 v62, v71
	v_mov_b32_e32 v63, v101
	v_mov_b32_dpp v12, v69 row_shr:1 row_mask:0xf bank_mask:0xf
	v_mov_b32_e32 v29, v69
	v_accvgpr_read_b32 v107, a37
	v_pk_fma_f32 v[60:61], v[62:63], v[24:25], v[60:61]
	v_pk_mul_f32 v[62:63], v[28:29], v[12:13]
	v_accvgpr_read_b32 v106, a36
	v_mov_b32_dpp v7, v68 row_shl:1 row_mask:0xf bank_mask:0xf
	v_pk_fma_f32 v[62:63], v[68:69], v[106:107], v[62:63] op_sel_hi:[0,1,1]
	v_mov_b32_e32 v68, v69
	v_mov_b32_e32 v69, v17
	v_mov_b32_e32 v78, v21
	v_pk_fma_f32 v[62:63], v[68:69], v[6:7], v[62:63]
	v_pk_add_f32 v[60:61], v[60:61], 0 op_sel_hi:[1,0]
	v_mov_b32_dpp v78, v83 row_shr:1 row_mask:0xf bank_mask:0xf
	v_mov_b32_e32 v53, v83
	v_accvgpr_read_b32 v14, a24
	v_pk_add_f32 v[60:61], v[60:61], v[62:63]
	v_pk_mul_f32 v[62:63], v[52:53], v[78:79]
	v_accvgpr_read_b32 v15, a25
	v_mov_b32_dpp v21, v82 row_shl:1 row_mask:0xf bank_mask:0xf
	v_pk_fma_f32 v[62:63], v[82:83], v[14:15], v[62:63] op_sel_hi:[0,1,1]
	v_mov_b32_e32 v68, v83
	v_mov_b32_e32 v69, v89
	v_pk_fma_f32 v[62:63], v[68:69], v[20:21], v[62:63]
	v_mov_b32_e32 v76, v11
	v_pk_add_f32 v[60:61], v[60:61], v[62:63]
	s_mov_b64 s[0:1], 0x410000
	v_mov_b32_dpp v76, v81 row_shr:1 row_mask:0xf bank_mask:0xf
	v_mov_b32_e32 v41, v81
	v_lshl_add_u64 v[136:137], v[134:135], 0, s[0:1]
	s_nop 1
	s_mov_b64 vcc, s[28:29]
	s_nop 0
	v_cndmask_b32_dpp v130, v60, v128, vcc quad_perm:[1,0,3,2] row_mask:0xf bank_mask:0xf
	v_cndmask_b32_dpp v131, v61, v129, vcc quad_perm:[1,0,3,2] row_mask:0xf bank_mask:0xf
	s_mov_b64 vcc, s[30:31]
	s_nop 0
	v_cndmask_b32_dpp v132, v128, v60, vcc quad_perm:[1,0,3,2] row_mask:0xf bank_mask:0xf
	v_cndmask_b32_dpp v133, v129, v61, vcc quad_perm:[1,0,3,2] row_mask:0xf bank_mask:0xf
	global_store_dwordx4 v[136:137], v[130:133], off sc0 sc1 nt
	s_nop 1
	v_pk_mul_f32 v[60:61], v[40:41], v[76:77]
	v_accvgpr_write_b32 a36, v66
	v_pk_fma_f32 v[60:61], v[80:81], v[66:67], v[60:61] op_sel_hi:[0,1,1]
	v_accvgpr_write_b32 a37, v67
	v_accvgpr_read_b32 v67, a29
	v_accvgpr_write_b32 a5, v2
	v_accvgpr_write_b32 a38, v100
	v_accvgpr_read_b32 v66, a28
	v_mov_b32_e32 v2, v35
	v_accvgpr_write_b32 a39, v101
	v_mov_b32_dpp v11, v80 row_shl:1 row_mask:0xf bank_mask:0xf
	v_pk_mov_b32 v[62:63], v[80:81], v[66:67] op_sel:[1,0]
	v_mov_b32_dpp v2, v85 row_shr:1 row_mask:0xf bank_mask:0xf
	v_mov_b32_e32 v23, v85
	v_accvgpr_read_b32 v101, a33
	v_pk_fma_f32 v[60:61], v[62:63], v[10:11], v[60:61]
	v_pk_mul_f32 v[62:63], v[22:23], v[2:3]
	v_accvgpr_read_b32 v100, a32
	v_mov_b32_dpp v35, v84 row_shl:1 row_mask:0xf bank_mask:0xf
	v_pk_fma_f32 v[62:63], v[84:85], v[100:101], v[62:63] op_sel_hi:[0,1,1]
	v_pk_mov_b32 v[68:69], v[84:85], v[8:9] op_sel:[1,0]
	v_mov_b32_e32 v92, v59
	v_pk_fma_f32 v[62:63], v[68:69], v[34:35], v[62:63]
	v_pk_add_f32 v[60:61], v[60:61], 0 op_sel_hi:[1,0]
	v_mov_b32_dpp v92, v127 row_shr:1 row_mask:0xf bank_mask:0xf
	v_mov_b32_e32 v97, v127
	v_accvgpr_read_b32 v17, a9
	v_accvgpr_read_b32 v71, a49
	v_pk_add_f32 v[60:61], v[60:61], v[62:63]
	v_pk_mul_f32 v[62:63], v[96:97], v[92:93]
	v_accvgpr_read_b32 v16, a8
	v_accvgpr_read_b32 v70, a48
	v_mov_b32_dpp v59, v126 row_shl:1 row_mask:0xf bank_mask:0xf
	v_pk_fma_f32 v[62:63], v[126:127], v[16:17], v[62:63] op_sel_hi:[0,1,1]
	v_pk_mov_b32 v[68:69], v[126:127], v[70:71] op_sel:[1,0]
	v_mov_b32_e32 v94, v57
	v_pk_fma_f32 v[62:63], v[68:69], v[58:59], v[62:63]
	v_accvgpr_write_b32 a20, v28
	v_pk_add_f32 v[60:61], v[60:61], v[62:63]
	s_mov_b64 s[0:1], 0x420000
	v_mov_b32_dpp v94, v125 row_shr:1 row_mask:0xf bank_mask:0xf
	v_mov_b32_e32 v99, v125
	v_accvgpr_read_b32 v29, a3
	v_lshl_add_u64 v[62:63], v[54:55], 0, s[0:1]
	v_mov_b32_e32 v128, v60
	v_mov_b32_e32 v129, v61
	v_pk_mul_f32 v[60:61], v[98:99], v[94:95]
	v_accvgpr_read_b32 v28, a2
	v_mov_b32_e32 v102, v51
	v_mov_b32_dpp v57, v124 row_shl:1 row_mask:0xf bank_mask:0xf
	v_pk_fma_f32 v[60:61], v[124:125], v[28:29], v[60:61] op_sel_hi:[0,1,1]
	v_mov_b32_e32 v62, v125
	v_mov_b32_e32 v63, v67
	v_mov_b32_dpp v102, v123 row_shr:1 row_mask:0xf bank_mask:0xf
	v_mov_b32_e32 v105, v123
	v_pk_fma_f32 v[60:61], v[62:63], v[56:57], v[60:61]
	v_pk_mul_f32 v[62:63], v[104:105], v[102:103]
	v_mov_b32_dpp v51, v122 row_shl:1 row_mask:0xf bank_mask:0xf
	v_pk_fma_f32 v[62:63], v[122:123], v[30:31], v[62:63] op_sel_hi:[0,1,1]
	v_accvgpr_write_b32 a28, v30
	v_mov_b32_e32 v68, v123
	v_mov_b32_e32 v69, v9
	v_mov_b32_e32 v108, v49
	v_accvgpr_write_b32 a29, v31
	v_pk_fma_f32 v[62:63], v[68:69], v[50:51], v[62:63]
	v_pk_add_f32 v[60:61], v[60:61], 0 op_sel_hi:[1,0]
	v_mov_b32_dpp v108, v121 row_shr:1 row_mask:0xf bank_mask:0xf
	v_mov_b32_e32 v111, v121
	v_accvgpr_read_b32 v31, a7
	v_pk_add_f32 v[60:61], v[60:61], v[62:63]
	v_pk_mul_f32 v[62:63], v[110:111], v[108:109]
	v_accvgpr_read_b32 v30, a6
	v_mov_b32_dpp v49, v120 row_shl:1 row_mask:0xf bank_mask:0xf
	v_pk_fma_f32 v[62:63], v[120:121], v[30:31], v[62:63] op_sel_hi:[0,1,1]
	v_mov_b32_e32 v68, v121
	v_mov_b32_e32 v69, v71
	v_pk_fma_f32 v[62:63], v[68:69], v[48:49], v[62:63]
	s_mov_b64 s[0:1], 0x430000
	v_pk_add_f32 v[60:61], v[60:61], v[62:63]
	v_lshl_add_u64 v[136:137], v[134:135], 0, s[0:1]
	v_add_u32_e32 v1, s16, v118
	s_add_u32 s0, s10, 0x1800000
	v_accvgpr_write_b32 a26, v114
	s_nop 1
	s_mov_b64 vcc, s[28:29]
	s_nop 0
	v_cndmask_b32_dpp v130, v60, v128, vcc quad_perm:[1,0,3,2] row_mask:0xf bank_mask:0xf
	v_cndmask_b32_dpp v131, v61, v129, vcc quad_perm:[1,0,3,2] row_mask:0xf bank_mask:0xf
	s_mov_b64 vcc, s[30:31]
	s_nop 0
	v_cndmask_b32_dpp v132, v128, v60, vcc quad_perm:[1,0,3,2] row_mask:0xf bank_mask:0xf
	v_cndmask_b32_dpp v133, v129, v61, vcc quad_perm:[1,0,3,2] row_mask:0xf bank_mask:0xf
	global_store_dwordx4 v[136:137], v[130:133], off sc0 sc1 nt
	s_nop 1
	v_readfirstlane_b32 s2, v1
	s_addc_u32 s1, s11, 0
	v_add_u32_e32 v1, s16, v90
	v_accvgpr_write_b32 a18, v116
	v_accvgpr_write_b32 a27, v115
	s_waitcnt vmcnt(16)
	v_lshl_add_u64 v[60:61], s[0:1], 0, v[32:33]
	s_mov_b32 m0, s2
	v_readfirstlane_b32 s2, v1
	v_add_u32_e32 v1, s16, v91
	v_accvgpr_read_b32 v115, a23
	v_accvgpr_write_b32 a19, v117
	s_waitcnt lgkmcnt(0)
	s_barrier
	global_load_lds_dwordx4 v[60:61], off nt
	v_lshl_add_u64 v[60:61], s[0:1], 0, v[74:75]
	s_mov_b32 m0, s2
	v_readfirstlane_b32 s2, v1
	v_accvgpr_read_b32 v114, a22
	v_add_u32_e32 v1, s16, v119
	v_accvgpr_read_b32 v117, a31
	global_load_lds_dwordx4 v[60:61], off nt
	v_lshl_add_u64 v[60:61], s[0:1], 0, v[114:115]
	s_mov_b32 m0, s2
	v_readfirstlane_b32 s2, v1
	v_accvgpr_read_b32 v116, a30
	global_load_lds_dwordx4 v[60:61], off nt
	v_lshl_add_u64 v[60:61], s[0:1], 0, v[116:117]
	s_mov_b32 m0, s2
	v_accvgpr_write_b32 a1, v5
	global_load_lds_dwordx4 v[60:61], off nt
	v_accvgpr_read_b32 v5, a10
	v_add_u32_e32 v2, 16, v5
	ds_read_b64 v[60:61], v2
	ds_read_b64 v[62:63], v2 offset:288
	ds_read_b64 v[68:69], v2 offset:576
	ds_read_b64 v[70:71], v2 offset:1728
	ds_read_b64 v[72:73], v2 offset:2016
	ds_read_b64 v[82:83], v2 offset:2304
	ds_read_b64 v[80:81], v2 offset:3456
	ds_read_b64 v[84:85], v2 offset:3744
	ds_read_b64 v[124:125], v2 offset:4032
	ds_read_b64 v[122:123], v2 offset:5184
	ds_read_b64 v[120:121], v2 offset:5472
	ds_read_b64 v[90:91], v2 offset:5760
	ds_read_b32 v43, v4
	ds_read_b32 v19, v4 offset:288
	ds_read_b32 v39, v4 offset:576
	ds_read_b32 v25, v4 offset:1728
	ds_read_b32 v7, v4 offset:2016
	ds_read_b32 v21, v4 offset:2304
	ds_read_b32 v11, v4 offset:3456
	ds_read_b32 v35, v4 offset:3744
	ds_read_b32 v59, v4 offset:4032
	ds_read_b32 v57, v4 offset:5184
	ds_read_b32 v51, v4 offset:5472
	ds_read_b32 v49, v4 offset:5760
	s_waitcnt lgkmcnt(0)
	v_accvgpr_write_b32 a46, v88
	v_mov_b32_e32 v46, v43
	v_accvgpr_write_b32 a8, v8
	v_mov_b32_e32 v113, v61
	v_mov_b32_dpp v46, v61 row_shr:1 row_mask:0xf bank_mask:0xf
	v_accvgpr_mov_b32 a42, a52
	v_accvgpr_write_b32 a47, v89
	v_accvgpr_write_b32 a9, v9
	v_pk_mul_f32 v[88:89], v[112:113], v[46:47]
	v_accvgpr_write_b32 a40, v112
	v_accvgpr_read_b32 v8, a18
	v_accvgpr_read_b32 v113, a39
	v_accvgpr_mov_b32 a43, a53
	v_accvgpr_write_b32 a51, v33
	v_accvgpr_write_b32 a52, v74
	v_accvgpr_read_b32 v9, a19
	v_accvgpr_read_b32 v112, a38
	v_mov_b32_e32 v26, v19
	v_accvgpr_write_b32 a50, v32
	v_accvgpr_write_b32 a53, v75
	v_mov_b32_dpp v43, v60 row_shl:1 row_mask:0xf bank_mask:0xf
	v_pk_fma_f32 v[88:89], v[60:61], v[8:9], v[88:89] op_sel_hi:[0,1,1]
	v_pk_mov_b32 v[60:61], v[60:61], v[112:113] op_sel:[1,0]
	v_mov_b32_dpp v26, v63 row_shr:1 row_mask:0xf bank_mask:0xf
	v_accvgpr_read_b32 v32, a34
	v_mov_b32_e32 v33, v63
	v_accvgpr_read_b32 v127, a27
	v_accvgpr_read_b32 v75, a43
	v_pk_fma_f32 v[60:61], v[60:61], v[42:43], v[88:89]
	v_pk_mul_f32 v[88:89], v[32:33], v[26:27]
	v_accvgpr_read_b32 v126, a26
	v_accvgpr_read_b32 v74, a42
	v_mov_b32_dpp v19, v62 row_shl:1 row_mask:0xf bank_mask:0xf
	v_pk_fma_f32 v[88:89], v[62:63], v[126:127], v[88:89] op_sel_hi:[0,1,1]
	v_pk_mov_b32 v[62:63], v[62:63], v[74:75] op_sel:[1,0]
	v_mov_b32_e32 v44, v39
	v_accvgpr_mov_b32 a14, a48
	v_pk_fma_f32 v[62:63], v[62:63], v[18:19], v[88:89]
	v_pk_add_f32 v[60:61], v[60:61], 0 op_sel_hi:[1,0]
	v_mov_b32_dpp v44, v69 row_shr:1 row_mask:0xf bank_mask:0xf
	v_mov_b32_e32 v1, v69
	v_accvgpr_mov_b32 a15, a49
	v_pk_add_f32 v[60:61], v[60:61], v[62:63]
	v_pk_mul_f32 v[62:63], v[0:1], v[44:45]
	v_accvgpr_write_b32 a48, v0
	v_accvgpr_read_b32 v89, a45
	v_accvgpr_read_b32 v0, a46
	v_accvgpr_read_b32 v88, a44
	v_accvgpr_read_b32 v1, a47
	v_mov_b32_dpp v39, v68 row_shl:1 row_mask:0xf bank_mask:0xf
	v_pk_fma_f32 v[62:63], v[68:69], v[88:89], v[62:63] op_sel_hi:[0,1,1]
	v_pk_mov_b32 v[68:69], v[68:69], v[0:1] op_sel:[1,0]
	v_mov_b32_e32 v36, v25
	v_pk_fma_f32 v[62:63], v[68:69], v[38:39], v[62:63]
	s_mov_b64 s[0:1], 0x800000
	v_pk_add_f32 v[60:61], v[60:61], v[62:63]
	v_mov_b32_dpp v36, v71 row_shr:1 row_mask:0xf bank_mask:0xf
	v_mov_b32_e32 v65, v71
	v_lshl_add_u64 v[62:63], v[54:55], 0, s[0:1]
	v_mov_b32_e32 v128, v60
	v_mov_b32_e32 v129, v61
	v_pk_mul_f32 v[60:61], v[64:65], v[36:37]
	v_mov_b64_e32 v[118:119], v[86:87]
	v_mov_b32_e32 v12, v7
	v_accvgpr_write_b32 a24, v32
	v_mov_b32_dpp v25, v70 row_shl:1 row_mask:0xf bank_mask:0xf
	v_pk_fma_f32 v[60:61], v[70:71], v[118:119], v[60:61] op_sel_hi:[0,1,1]
	v_mov_b32_e32 v62, v71
	v_mov_b32_e32 v63, v113
	v_mov_b32_dpp v12, v73 row_shr:1 row_mask:0xf bank_mask:0xf
	v_accvgpr_read_b32 v32, a20
	v_mov_b32_e32 v33, v73
	v_pk_fma_f32 v[60:61], v[62:63], v[24:25], v[60:61]
	v_pk_mul_f32 v[62:63], v[32:33], v[12:13]
	v_mov_b32_dpp v7, v72 row_shl:1 row_mask:0xf bank_mask:0xf
	v_pk_fma_f32 v[62:63], v[72:73], v[106:107], v[62:63] op_sel_hi:[0,1,1]
	v_mov_b32_e32 v68, v73
	v_mov_b32_e32 v69, v75
	v_mov_b32_e32 v78, v21
	v_pk_fma_f32 v[62:63], v[68:69], v[6:7], v[62:63]
	v_pk_add_f32 v[60:61], v[60:61], 0 op_sel_hi:[1,0]
	v_mov_b32_dpp v78, v83 row_shr:1 row_mask:0xf bank_mask:0xf
	v_mov_b32_e32 v53, v83
	v_pk_add_f32 v[60:61], v[60:61], v[62:63]
	v_pk_mul_f32 v[62:63], v[52:53], v[78:79]
	v_mov_b32_dpp v21, v82 row_shl:1 row_mask:0xf bank_mask:0xf
	v_pk_fma_f32 v[62:63], v[82:83], v[14:15], v[62:63] op_sel_hi:[0,1,1]
	v_mov_b32_e32 v68, v83
	v_mov_b32_e32 v69, v1
	v_accvgpr_write_b32 a19, v15
	v_pk_fma_f32 v[62:63], v[68:69], v[20:21], v[62:63]
	v_mov_b32_e32 v76, v11
	v_accvgpr_write_b32 a18, v14
	v_pk_add_f32 v[60:61], v[60:61], v[62:63]
	s_mov_b64 s[0:1], 0x810000
	v_mov_b32_dpp v76, v81 row_shr:1 row_mask:0xf bank_mask:0xf
	v_mov_b32_e32 v41, v81
	v_accvgpr_read_b32 v14, a36
	v_accvgpr_write_b32 a6, v2
	v_lshl_add_u64 v[136:137], v[134:135], 0, s[0:1]
	s_nop 1
	s_mov_b64 vcc, s[28:29]
	s_nop 0
	v_cndmask_b32_dpp v130, v60, v128, vcc quad_perm:[1,0,3,2] row_mask:0xf bank_mask:0xf
	v_cndmask_b32_dpp v131, v61, v129, vcc quad_perm:[1,0,3,2] row_mask:0xf bank_mask:0xf
	s_mov_b64 vcc, s[30:31]
	s_nop 0
	v_cndmask_b32_dpp v132, v128, v60, vcc quad_perm:[1,0,3,2] row_mask:0xf bank_mask:0xf
	v_cndmask_b32_dpp v133, v129, v61, vcc quad_perm:[1,0,3,2] row_mask:0xf bank_mask:0xf
	global_store_dwordx4 v[136:137], v[130:133], off sc0 sc1 nt
	s_nop 1
	v_pk_mul_f32 v[60:61], v[40:41], v[76:77]
	v_accvgpr_read_b32 v15, a37
	v_mov_b32_e32 v2, v35
	v_mov_b32_dpp v11, v80 row_shl:1 row_mask:0xf bank_mask:0xf
	v_pk_fma_f32 v[60:61], v[80:81], v[14:15], v[60:61] op_sel_hi:[0,1,1]
	v_pk_mov_b32 v[62:63], v[80:81], v[66:67] op_sel:[1,0]
	v_mov_b32_dpp v2, v85 row_shr:1 row_mask:0xf bank_mask:0xf
	v_mov_b32_e32 v23, v85
	v_accvgpr_read_b32 v15, a9
	v_pk_fma_f32 v[60:61], v[62:63], v[10:11], v[60:61]
	v_pk_mul_f32 v[62:63], v[22:23], v[2:3]
	v_accvgpr_read_b32 v14, a8
	v_mov_b32_dpp v35, v84 row_shl:1 row_mask:0xf bank_mask:0xf
	v_pk_fma_f32 v[62:63], v[84:85], v[100:101], v[62:63] op_sel_hi:[0,1,1]
	v_pk_mov_b32 v[68:69], v[84:85], v[14:15] op_sel:[1,0]
	v_mov_b32_e32 v92, v59
	v_pk_fma_f32 v[62:63], v[68:69], v[34:35], v[62:63]
	v_pk_add_f32 v[60:61], v[60:61], 0 op_sel_hi:[1,0]
	v_mov_b32_dpp v92, v125 row_shr:1 row_mask:0xf bank_mask:0xf
	v_mov_b32_e32 v97, v125
	v_accvgpr_read_b32 v71, a15
	v_pk_add_f32 v[60:61], v[60:61], v[62:63]
	v_pk_mul_f32 v[62:63], v[96:97], v[92:93]
	v_accvgpr_read_b32 v70, a14
	v_mov_b32_dpp v59, v124 row_shl:1 row_mask:0xf bank_mask:0xf
	v_pk_fma_f32 v[62:63], v[124:125], v[16:17], v[62:63] op_sel_hi:[0,1,1]
	v_pk_mov_b32 v[68:69], v[124:125], v[70:71] op_sel:[1,0]
	v_mov_b32_e32 v94, v57
	v_pk_fma_f32 v[62:63], v[68:69], v[58:59], v[62:63]
	s_mov_b64 s[0:1], 0x820000
	v_pk_add_f32 v[60:61], v[60:61], v[62:63]
	v_mov_b32_dpp v94, v123 row_shr:1 row_mask:0xf bank_mask:0xf
	v_mov_b32_e32 v99, v123
	v_accvgpr_write_b32 a31, v17
	v_lshl_add_u64 v[62:63], v[54:55], 0, s[0:1]
	v_mov_b32_e32 v128, v60
	v_mov_b32_e32 v129, v61
	v_pk_mul_f32 v[60:61], v[98:99], v[94:95]
	v_mov_b32_e32 v102, v51
	v_accvgpr_write_b32 a30, v16
	v_mov_b32_dpp v57, v122 row_shl:1 row_mask:0xf bank_mask:0xf
	v_pk_fma_f32 v[60:61], v[122:123], v[28:29], v[60:61] op_sel_hi:[0,1,1]
	v_mov_b32_e32 v62, v123
	v_mov_b32_e32 v63, v67
	v_mov_b32_dpp v102, v121 row_shr:1 row_mask:0xf bank_mask:0xf
	v_mov_b32_e32 v105, v121
	v_accvgpr_read_b32 v16, a28
	v_pk_fma_f32 v[60:61], v[62:63], v[56:57], v[60:61]
	v_pk_mul_f32 v[62:63], v[104:105], v[102:103]
	v_accvgpr_read_b32 v17, a29
	v_mov_b32_dpp v51, v120 row_shl:1 row_mask:0xf bank_mask:0xf
	v_pk_fma_f32 v[62:63], v[120:121], v[16:17], v[62:63] op_sel_hi:[0,1,1]
	v_mov_b32_e32 v68, v121
	v_mov_b32_e32 v69, v15
	v_mov_b32_e32 v108, v49
	v_pk_fma_f32 v[62:63], v[68:69], v[50:51], v[62:63]
	v_pk_add_f32 v[60:61], v[60:61], 0 op_sel_hi:[1,0]
	v_mov_b32_dpp v108, v91 row_shr:1 row_mask:0xf bank_mask:0xf
	v_mov_b32_e32 v111, v91
	v_pk_add_f32 v[60:61], v[60:61], v[62:63]
	v_pk_mul_f32 v[62:63], v[110:111], v[108:109]
	v_mov_b32_dpp v49, v90 row_shl:1 row_mask:0xf bank_mask:0xf
	v_pk_fma_f32 v[62:63], v[90:91], v[30:31], v[62:63] op_sel_hi:[0,1,1]
	v_mov_b32_e32 v68, v91
	v_mov_b32_e32 v69, v71
	v_pk_fma_f32 v[62:63], v[68:69], v[48:49], v[62:63]
	s_mov_b64 s[0:1], 0x830000
	v_mov_b32_e32 v0, v22
	v_pk_add_f32 v[60:61], v[60:61], v[62:63]
	v_lshl_add_u64 v[136:137], v[134:135], 0, s[0:1]
	s_add_u32 s0, s10, 0x1c00000
	v_accvgpr_read_b32 v22, a50
	v_accvgpr_read_b32 v1, a72
	s_addc_u32 s1, s11, 0
	v_accvgpr_read_b32 v23, a51
	s_nop 1
	s_mov_b64 vcc, s[28:29]
	s_nop 0
	v_cndmask_b32_dpp v130, v60, v128, vcc quad_perm:[1,0,3,2] row_mask:0xf bank_mask:0xf
	v_cndmask_b32_dpp v131, v61, v129, vcc quad_perm:[1,0,3,2] row_mask:0xf bank_mask:0xf
	s_mov_b64 vcc, s[30:31]
	s_nop 0
	v_cndmask_b32_dpp v132, v128, v60, vcc quad_perm:[1,0,3,2] row_mask:0xf bank_mask:0xf
	v_cndmask_b32_dpp v133, v129, v61, vcc quad_perm:[1,0,3,2] row_mask:0xf bank_mask:0xf
	global_store_dwordx4 v[136:137], v[130:133], off sc0 sc1 nt
	s_nop 1
	v_readfirstlane_b32 s2, v1
	v_lshl_add_u64 v[60:61], s[0:1], 0, v[22:23]
	v_accvgpr_read_b32 v1, a12
	v_accvgpr_read_b32 v22, a52
	s_waitcnt vmcnt(18)
	s_mov_b32 m0, s2
	v_readfirstlane_b32 s2, v1
	v_accvgpr_read_b32 v23, a53
	v_accvgpr_read_b32 v1, a13
	s_waitcnt lgkmcnt(0)
	s_barrier
	global_load_lds_dwordx4 v[60:61], off nt
	v_lshl_add_u64 v[60:61], s[0:1], 0, v[22:23]
	s_mov_b32 m0, s2
	v_readfirstlane_b32 s2, v1
	v_accvgpr_read_b32 v1, a16
	global_load_lds_dwordx4 v[60:61], off nt
	v_lshl_add_u64 v[60:61], s[0:1], 0, v[114:115]
	s_mov_b32 m0, s2
	v_readfirstlane_b32 s2, v1
	global_load_lds_dwordx4 v[60:61], off nt
	v_lshl_add_u64 v[60:61], s[0:1], 0, v[116:117]
	s_mov_b32 m0, s2
	v_accvgpr_write_b32 a22, v30
	v_accvgpr_write_b32 a44, v70
	global_load_lds_dwordx4 v[60:61], off nt
	v_accvgpr_write_b32 a2, v106
	v_accvgpr_write_b32 a34, v74
	v_accvgpr_write_b32 a23, v31
	v_accvgpr_write_b32 a45, v71
	v_add_u32_e32 v2, 0x7010, v5
	v_mov_b32_e32 v31, v5
	v_add_u32_e32 v5, 0x7000, v4
	ds_read_b64 v[60:61], v2
	ds_read_b64 v[62:63], v2 offset:288
	ds_read_b64 v[68:69], v2 offset:576
	ds_read_b64 v[70:71], v2 offset:1728
	ds_read_b64 v[72:73], v2 offset:2016
	ds_read_b64 v[82:83], v2 offset:2304
	ds_read_b64 v[80:81], v2 offset:3456
	ds_read_b64 v[84:85], v2 offset:3744
	ds_read_b64 v[116:117], v2 offset:4032
	ds_read_b64 v[114:115], v2 offset:5184
	ds_read_b64 v[112:113], v2 offset:5472
	ds_read_b64 v[90:91], v2 offset:5760
	ds_read_b32 v43, v5
	ds_read_b32 v19, v5 offset:288
	ds_read_b32 v39, v5 offset:576
	ds_read_b32 v25, v5 offset:1728
	ds_read_b32 v7, v5 offset:2016
	ds_read_b32 v21, v5 offset:2304
	ds_read_b32 v11, v5 offset:3456
	ds_read_b32 v35, v5 offset:3744
	ds_read_b32 v59, v5 offset:4032
	ds_read_b32 v57, v5 offset:5184
	ds_read_b32 v51, v5 offset:5472
	ds_read_b32 v49, v5 offset:5760
	s_waitcnt lgkmcnt(0)
	v_accvgpr_write_b32 a3, v107
	v_mov_b32_e32 v46, v43
	v_accvgpr_write_b32 a35, v75
	v_accvgpr_read_b32 v74, a40
	v_mov_b32_dpp v46, v61 row_shr:1 row_mask:0xf bank_mask:0xf
	v_mov_b32_e32 v75, v61
	v_accvgpr_read_b32 v107, a39
	v_accvgpr_write_b32 a10, v100
	v_pk_mul_f32 v[86:87], v[74:75], v[46:47]
	v_accvgpr_read_b32 v106, a38
	v_mov_b32_e32 v26, v19
	v_accvgpr_write_b32 a11, v101
	v_mov_b32_dpp v43, v60 row_shl:1 row_mask:0xf bank_mask:0xf
	v_mov_b32_e32 v32, v74
	v_pk_fma_f32 v[86:87], v[60:61], v[8:9], v[86:87] op_sel_hi:[0,1,1]
	v_pk_mov_b32 v[60:61], v[60:61], v[106:107] op_sel:[1,0]
	v_mov_b32_dpp v26, v63 row_shr:1 row_mask:0xf bank_mask:0xf
	v_accvgpr_read_b32 v74, a24
	v_mov_b32_e32 v75, v63
	v_accvgpr_read_b32 v101, a35
	v_pk_fma_f32 v[60:61], v[60:61], v[42:43], v[86:87]
	v_pk_mul_f32 v[86:87], v[74:75], v[26:27]
	v_accvgpr_read_b32 v100, a34
	v_accvgpr_write_b32 a14, v66
	v_mov_b32_dpp v19, v62 row_shl:1 row_mask:0xf bank_mask:0xf
	v_pk_fma_f32 v[86:87], v[62:63], v[126:127], v[86:87] op_sel_hi:[0,1,1]
	v_pk_mov_b32 v[62:63], v[62:63], v[100:101] op_sel:[1,0]
	v_mov_b32_e32 v44, v39
	v_accvgpr_write_b32 a42, v64
	v_accvgpr_write_b32 a15, v67
	v_mov_b32_e32 v66, v4
	v_pk_fma_f32 v[62:63], v[62:63], v[18:19], v[86:87]
	v_pk_add_f32 v[60:61], v[60:61], 0 op_sel_hi:[1,0]
	v_mov_b32_dpp v44, v69 row_shr:1 row_mask:0xf bank_mask:0xf
	v_accvgpr_read_b32 v64, a48
	v_mov_b32_e32 v65, v69
	v_accvgpr_read_b32 v4, a46
	v_pk_add_f32 v[60:61], v[60:61], v[62:63]
	v_pk_mul_f32 v[62:63], v[64:65], v[44:45]
	v_accvgpr_read_b32 v5, a47
	v_mov_b32_dpp v39, v68 row_shl:1 row_mask:0xf bank_mask:0xf
	v_pk_fma_f32 v[62:63], v[68:69], v[88:89], v[62:63] op_sel_hi:[0,1,1]
	v_pk_mov_b32 v[68:69], v[68:69], v[4:5] op_sel:[1,0]
	v_mov_b32_e32 v36, v25
	v_pk_fma_f32 v[62:63], v[68:69], v[38:39], v[62:63]
	s_mov_b64 s[0:1], 0xc00000
	v_pk_add_f32 v[60:61], v[60:61], v[62:63]
	v_mov_b32_dpp v36, v71 row_shr:1 row_mask:0xf bank_mask:0xf
	v_accvgpr_read_b32 v22, a42
	v_mov_b32_e32 v23, v71
	v_accvgpr_mov_b32 a26, a20
	v_accvgpr_write_b32 a20, v28
	v_lshl_add_u64 v[62:63], v[54:55], 0, s[0:1]
	v_mov_b32_e32 v128, v60
	v_mov_b32_e32 v129, v61
	v_pk_mul_f32 v[60:61], v[22:23], v[36:37]
	v_mov_b32_e32 v12, v7
	v_accvgpr_write_b32 a21, v29
	v_mov_b32_dpp v25, v70 row_shl:1 row_mask:0xf bank_mask:0xf
	v_pk_fma_f32 v[60:61], v[70:71], v[118:119], v[60:61] op_sel_hi:[0,1,1]
	v_mov_b32_e32 v62, v71
	v_mov_b32_e32 v63, v107
	v_mov_b32_dpp v12, v73 row_shr:1 row_mask:0xf bank_mask:0xf
	v_accvgpr_read_b32 v28, a26
	v_mov_b32_e32 v29, v73
	v_accvgpr_read_b32 v121, a3
	v_pk_fma_f32 v[60:61], v[62:63], v[24:25], v[60:61]
	v_pk_mul_f32 v[62:63], v[28:29], v[12:13]
	v_accvgpr_read_b32 v120, a2
	v_mov_b32_dpp v7, v72 row_shl:1 row_mask:0xf bank_mask:0xf
	v_pk_fma_f32 v[62:63], v[72:73], v[120:121], v[62:63] op_sel_hi:[0,1,1]
	v_mov_b32_e32 v68, v73
	v_mov_b32_e32 v69, v101
	v_mov_b32_e32 v78, v21
	v_pk_fma_f32 v[62:63], v[68:69], v[6:7], v[62:63]
	v_pk_add_f32 v[60:61], v[60:61], 0 op_sel_hi:[1,0]
	v_mov_b32_dpp v78, v83 row_shr:1 row_mask:0xf bank_mask:0xf
	v_mov_b32_e32 v53, v83
	v_accvgpr_read_b32 v125, a19
	v_pk_add_f32 v[60:61], v[60:61], v[62:63]
	v_pk_mul_f32 v[62:63], v[52:53], v[78:79]
	v_accvgpr_read_b32 v124, a18
	v_mov_b32_dpp v21, v82 row_shl:1 row_mask:0xf bank_mask:0xf
	v_pk_fma_f32 v[62:63], v[82:83], v[124:125], v[62:63] op_sel_hi:[0,1,1]
	v_mov_b32_e32 v68, v83
	v_mov_b32_e32 v69, v5
	v_pk_fma_f32 v[62:63], v[68:69], v[20:21], v[62:63]
	v_mov_b32_e32 v76, v11
	v_pk_add_f32 v[60:61], v[60:61], v[62:63]
	s_mov_b64 s[0:1], 0xc10000
	v_mov_b32_dpp v76, v81 row_shr:1 row_mask:0xf bank_mask:0xf
	v_mov_b32_e32 v41, v81
	v_accvgpr_read_b32 v123, a37
	v_accvgpr_read_b32 v4, a14
	v_lshl_add_u64 v[136:137], v[134:135], 0, s[0:1]
	s_nop 1
	s_mov_b64 vcc, s[28:29]
	s_nop 0
	v_cndmask_b32_dpp v130, v60, v128, vcc quad_perm:[1,0,3,2] row_mask:0xf bank_mask:0xf
	v_cndmask_b32_dpp v131, v61, v129, vcc quad_perm:[1,0,3,2] row_mask:0xf bank_mask:0xf
	s_mov_b64 vcc, s[30:31]
	s_nop 0
	v_cndmask_b32_dpp v132, v128, v60, vcc quad_perm:[1,0,3,2] row_mask:0xf bank_mask:0xf
	v_cndmask_b32_dpp v133, v129, v61, vcc quad_perm:[1,0,3,2] row_mask:0xf bank_mask:0xf
	global_store_dwordx4 v[136:137], v[130:133], off sc0 sc1 nt
	s_nop 1
	v_pk_mul_f32 v[60:61], v[40:41], v[76:77]
	v_accvgpr_read_b32 v122, a36
	v_accvgpr_read_b32 v5, a15
	v_mov_b32_e32 v2, v35
	v_accvgpr_mov_b32 a32, a24
	v_accvgpr_write_b32 a24, v22
	v_mov_b64_e32 v[22:23], v[118:119]
	v_mov_b32_dpp v11, v80 row_shl:1 row_mask:0xf bank_mask:0xf
	v_pk_fma_f32 v[60:61], v[80:81], v[122:123], v[60:61] op_sel_hi:[0,1,1]
	v_pk_mov_b32 v[62:63], v[80:81], v[4:5] op_sel:[1,0]
	v_mov_b32_dpp v2, v85 row_shr:1 row_mask:0xf bank_mask:0xf
	v_mov_b32_e32 v106, v0
	v_mov_b32_e32 v107, v85
	v_accvgpr_read_b32 v119, a11
	v_pk_fma_f32 v[60:61], v[62:63], v[10:11], v[60:61]
	v_pk_mul_f32 v[62:63], v[106:107], v[2:3]
	v_accvgpr_read_b32 v118, a10
	v_mov_b64_e32 v[100:101], v[14:15]
	v_mov_b32_dpp v35, v84 row_shl:1 row_mask:0xf bank_mask:0xf
	v_pk_fma_f32 v[62:63], v[84:85], v[118:119], v[62:63] op_sel_hi:[0,1,1]
	v_pk_mov_b32 v[68:69], v[84:85], v[100:101] op_sel:[1,0]
	v_mov_b32_e32 v92, v59
	v_accvgpr_write_b32 a26, v52
	v_mov_b32_e32 v74, v40
	v_pk_fma_f32 v[62:63], v[68:69], v[34:35], v[62:63]
	v_pk_add_f32 v[60:61], v[60:61], 0 op_sel_hi:[1,0]
	v_mov_b32_dpp v92, v117 row_shr:1 row_mask:0xf bank_mask:0xf
	v_mov_b32_e32 v97, v117
	v_accvgpr_read_b32 v41, a31
	v_accvgpr_read_b32 v53, a45
	v_pk_add_f32 v[60:61], v[60:61], v[62:63]
	v_pk_mul_f32 v[62:63], v[96:97], v[92:93]
	v_accvgpr_read_b32 v40, a30
	v_accvgpr_read_b32 v52, a44
	v_mov_b32_dpp v59, v116 row_shl:1 row_mask:0xf bank_mask:0xf
	v_pk_fma_f32 v[62:63], v[116:117], v[40:41], v[62:63] op_sel_hi:[0,1,1]
	v_pk_mov_b32 v[68:69], v[116:117], v[52:53] op_sel:[1,0]
	v_mov_b32_e32 v94, v57
	v_pk_fma_f32 v[62:63], v[68:69], v[58:59], v[62:63]
	s_mov_b64 s[0:1], 0xc20000
	v_pk_add_f32 v[60:61], v[60:61], v[62:63]
	v_mov_b32_dpp v94, v115 row_shr:1 row_mask:0xf bank_mask:0xf
	v_mov_b32_e32 v99, v115
	v_accvgpr_read_b32 v14, a20
	v_lshl_add_u64 v[62:63], v[54:55], 0, s[0:1]
	v_mov_b32_e32 v128, v60
	v_mov_b32_e32 v129, v61
	v_pk_mul_f32 v[60:61], v[98:99], v[94:95]
	v_accvgpr_read_b32 v15, a21
	v_mov_b32_e32 v102, v51
	v_mov_b32_dpp v57, v114 row_shl:1 row_mask:0xf bank_mask:0xf
	v_pk_fma_f32 v[60:61], v[114:115], v[14:15], v[60:61] op_sel_hi:[0,1,1]
	v_mov_b32_e32 v62, v115
	v_mov_b32_e32 v63, v5
	v_mov_b32_dpp v102, v113 row_shr:1 row_mask:0xf bank_mask:0xf
	v_mov_b32_e32 v105, v113
	v_pk_fma_f32 v[60:61], v[62:63], v[56:57], v[60:61]
	v_pk_mul_f32 v[62:63], v[104:105], v[102:103]
	v_accvgpr_write_b32 a8, v8
	v_mov_b32_dpp v51, v112 row_shl:1 row_mask:0xf bank_mask:0xf
	v_pk_fma_f32 v[62:63], v[112:113], v[16:17], v[62:63] op_sel_hi:[0,1,1]
	v_mov_b32_e32 v68, v113
	v_mov_b32_e32 v69, v101
	v_mov_b32_e32 v108, v49
	v_accvgpr_write_b32 a9, v9
	v_pk_fma_f32 v[62:63], v[68:69], v[50:51], v[62:63]
	v_pk_add_f32 v[60:61], v[60:61], 0 op_sel_hi:[1,0]
	v_mov_b32_dpp v108, v91 row_shr:1 row_mask:0xf bank_mask:0xf
	v_mov_b32_e32 v111, v91
	v_accvgpr_read_b32 v8, a22
	v_pk_add_f32 v[60:61], v[60:61], v[62:63]
	v_pk_mul_f32 v[62:63], v[110:111], v[108:109]
	v_accvgpr_read_b32 v9, a23
	v_mov_b32_dpp v49, v90 row_shl:1 row_mask:0xf bank_mask:0xf
	v_pk_fma_f32 v[62:63], v[90:91], v[8:9], v[62:63] op_sel_hi:[0,1,1]
	v_mov_b32_e32 v68, v91
	v_mov_b32_e32 v69, v53
	v_pk_fma_f32 v[62:63], v[68:69], v[48:49], v[62:63]
	s_mov_b64 s[0:1], 0xc30000
	v_pk_add_f32 v[60:61], v[60:61], v[62:63]
	v_lshl_add_u64 v[136:137], v[134:135], 0, s[0:1]
	s_nop 1
	s_mov_b64 vcc, s[28:29]
	s_nop 0
	v_cndmask_b32_dpp v130, v60, v128, vcc quad_perm:[1,0,3,2] row_mask:0xf bank_mask:0xf
	v_cndmask_b32_dpp v131, v61, v129, vcc quad_perm:[1,0,3,2] row_mask:0xf bank_mask:0xf
	s_mov_b64 vcc, s[30:31]
	s_nop 0
	v_cndmask_b32_dpp v132, v128, v60, vcc quad_perm:[1,0,3,2] row_mask:0xf bank_mask:0xf
	v_cndmask_b32_dpp v133, v129, v61, vcc quad_perm:[1,0,3,2] row_mask:0xf bank_mask:0xf
	global_store_dwordx4 v[136:137], v[130:133], off sc0 sc1 nt
	s_nop 1
	s_waitcnt vmcnt(20)
	v_accvgpr_write_b32 a16, v88
	v_accvgpr_write_b32 a10, v100
	s_waitcnt lgkmcnt(0)
	s_barrier
	v_add_u32_e32 v2, 0xe010, v31
	v_add_u32_e32 v5, 0xe000, v66
	ds_read_b64 v[60:61], v2
	ds_read_b64 v[62:63], v2 offset:288
	ds_read_b64 v[68:69], v2 offset:576
	ds_read_b64 v[70:71], v2 offset:1728
	ds_read_b64 v[72:73], v2 offset:2016
	ds_read_b64 v[82:83], v2 offset:2304
	ds_read_b64 v[80:81], v2 offset:3456
	ds_read_b64 v[84:85], v2 offset:3744
	ds_read_b64 v[116:117], v2 offset:4032
	ds_read_b64 v[114:115], v2 offset:5184
	ds_read_b64 v[112:113], v2 offset:5472
	ds_read_b64 v[90:91], v2 offset:5760
	ds_read_b32 v43, v5
	ds_read_b32 v19, v5 offset:288
	ds_read_b32 v39, v5 offset:576
	ds_read_b32 v25, v5 offset:1728
	ds_read_b32 v7, v5 offset:2016
	ds_read_b32 v21, v5 offset:2304
	ds_read_b32 v11, v5 offset:3456
	ds_read_b32 v35, v5 offset:3744
	ds_read_b32 v59, v5 offset:4032
	ds_read_b32 v57, v5 offset:5184
	ds_read_b32 v51, v5 offset:5472
	ds_read_b32 v49, v5 offset:5760
	s_waitcnt lgkmcnt(0)
	v_accvgpr_write_b32 a17, v89
	v_mov_b32_e32 v46, v43
	v_accvgpr_write_b32 a11, v101
	v_mov_b32_e32 v33, v61
	v_mov_b32_dpp v46, v61 row_shr:1 row_mask:0xf bank_mask:0xf
	v_accvgpr_read_b32 v89, a9
	v_accvgpr_read_b32 v101, a39
	v_pk_mul_f32 v[86:87], v[32:33], v[46:47]
	v_accvgpr_read_b32 v88, a8
	v_accvgpr_read_b32 v100, a38
	v_mov_b32_e32 v26, v19
	v_accvgpr_write_b32 a19, v17
	v_mov_b32_dpp v43, v60 row_shl:1 row_mask:0xf bank_mask:0xf
	v_pk_fma_f32 v[86:87], v[60:61], v[88:89], v[86:87] op_sel_hi:[0,1,1]
	v_pk_mov_b32 v[60:61], v[60:61], v[100:101] op_sel:[1,0]
	v_mov_b32_dpp v26, v63 row_shr:1 row_mask:0xf bank_mask:0xf
	v_accvgpr_read_b32 v0, a32
	v_mov_b32_e32 v1, v63
	v_accvgpr_read_b32 v4, a34
	v_accvgpr_write_b32 a18, v16
	v_pk_fma_f32 v[60:61], v[60:61], v[42:43], v[86:87]
	v_pk_mul_f32 v[86:87], v[0:1], v[26:27]
	v_mov_b64_e32 v[16:17], v[126:127]
	v_accvgpr_read_b32 v5, a35
	v_mov_b32_dpp v19, v62 row_shl:1 row_mask:0xf bank_mask:0xf
	v_pk_fma_f32 v[86:87], v[62:63], v[16:17], v[86:87] op_sel_hi:[0,1,1]
	v_pk_mov_b32 v[62:63], v[62:63], v[4:5] op_sel:[1,0]
	v_mov_b32_e32 v44, v39
	v_accvgpr_read_b32 v30, a48
	v_mov_b32_e32 v64, v28
	v_accvgpr_write_b32 a7, v66
	v_pk_fma_f32 v[62:63], v[62:63], v[18:19], v[86:87]
	v_pk_add_f32 v[60:61], v[60:61], 0 op_sel_hi:[1,0]
	v_mov_b32_dpp v44, v69 row_shr:1 row_mask:0xf bank_mask:0xf
	v_mov_b32_e32 v31, v69
	v_accvgpr_read_b32 v29, a17
	v_accvgpr_read_b32 v67, a47
	v_pk_add_f32 v[60:61], v[60:61], v[62:63]
	v_pk_mul_f32 v[62:63], v[30:31], v[44:45]
	v_accvgpr_read_b32 v28, a16
	v_accvgpr_read_b32 v66, a46
	v_mov_b32_dpp v39, v68 row_shl:1 row_mask:0xf bank_mask:0xf
	v_pk_fma_f32 v[62:63], v[68:69], v[28:29], v[62:63] op_sel_hi:[0,1,1]
	v_pk_mov_b32 v[68:69], v[68:69], v[66:67] op_sel:[1,0]
	v_mov_b32_e32 v36, v25
	v_pk_fma_f32 v[62:63], v[68:69], v[38:39], v[62:63]
	s_mov_b64 s[0:1], 0x1000000
	v_pk_add_f32 v[60:61], v[60:61], v[62:63]
	v_mov_b32_dpp v36, v71 row_shr:1 row_mask:0xf bank_mask:0xf
	v_accvgpr_read_b32 v126, a24
	v_mov_b32_e32 v127, v71
	v_lshl_add_u64 v[62:63], v[54:55], 0, s[0:1]
	v_mov_b32_e32 v128, v60
	v_mov_b32_e32 v129, v61
	v_pk_mul_f32 v[60:61], v[126:127], v[36:37]
	v_mov_b32_e32 v12, v7
	v_mov_b32_dpp v25, v70 row_shl:1 row_mask:0xf bank_mask:0xf
	v_pk_fma_f32 v[60:61], v[70:71], v[22:23], v[60:61] op_sel_hi:[0,1,1]
	v_mov_b32_e32 v62, v71
	v_mov_b32_e32 v63, v101
	v_mov_b32_dpp v12, v73 row_shr:1 row_mask:0xf bank_mask:0xf
	v_mov_b32_e32 v52, v64
	v_mov_b32_e32 v53, v73
	v_pk_fma_f32 v[60:61], v[62:63], v[24:25], v[60:61]
	v_pk_mul_f32 v[62:63], v[52:53], v[12:13]
	v_mov_b32_dpp v7, v72 row_shl:1 row_mask:0xf bank_mask:0xf
	v_pk_fma_f32 v[62:63], v[72:73], v[120:121], v[62:63] op_sel_hi:[0,1,1]
	v_mov_b32_e32 v68, v73
	v_mov_b32_e32 v69, v5
	v_mov_b32_e32 v78, v21
	v_pk_fma_f32 v[62:63], v[68:69], v[6:7], v[62:63]
	v_pk_add_f32 v[60:61], v[60:61], 0 op_sel_hi:[1,0]
	v_mov_b32_dpp v78, v83 row_shr:1 row_mask:0xf bank_mask:0xf
	v_accvgpr_read_b32 v4, a26
	v_mov_b32_e32 v5, v83
	v_pk_add_f32 v[60:61], v[60:61], v[62:63]
	v_pk_mul_f32 v[62:63], v[4:5], v[78:79]
	v_mov_b32_dpp v21, v82 row_shl:1 row_mask:0xf bank_mask:0xf
	v_pk_fma_f32 v[62:63], v[82:83], v[124:125], v[62:63] op_sel_hi:[0,1,1]
	v_mov_b32_e32 v68, v83
	v_mov_b32_e32 v69, v67
	v_accvgpr_write_b32 a8, v120
	v_pk_fma_f32 v[62:63], v[68:69], v[20:21], v[62:63]
	v_mov_b32_e32 v76, v11
	v_accvgpr_write_b32 a9, v121
	v_pk_add_f32 v[60:61], v[60:61], v[62:63]
	s_mov_b64 s[0:1], 0x1010000
	v_mov_b32_dpp v76, v81 row_shr:1 row_mask:0xf bank_mask:0xf
	v_mov_b32_e32 v120, v74
	v_mov_b32_e32 v121, v81
	v_accvgpr_read_b32 v101, a15
	v_accvgpr_mov_b32 a12, a38
	v_lshl_add_u64 v[136:137], v[134:135], 0, s[0:1]
	s_nop 1
	s_mov_b64 vcc, s[28:29]
	s_nop 0
	v_cndmask_b32_dpp v130, v60, v128, vcc quad_perm:[1,0,3,2] row_mask:0xf bank_mask:0xf
	v_cndmask_b32_dpp v131, v61, v129, vcc quad_perm:[1,0,3,2] row_mask:0xf bank_mask:0xf
	s_mov_b64 vcc, s[30:31]
	s_nop 0
	v_cndmask_b32_dpp v132, v128, v60, vcc quad_perm:[1,0,3,2] row_mask:0xf bank_mask:0xf
	v_cndmask_b32_dpp v133, v129, v61, vcc quad_perm:[1,0,3,2] row_mask:0xf bank_mask:0xf
	global_store_dwordx4 v[136:137], v[130:133], off sc0 sc1 nt
	s_nop 1
	v_pk_mul_f32 v[60:61], v[120:121], v[76:77]
	v_accvgpr_read_b32 v100, a14
	v_mov_b32_e32 v2, v35
	v_accvgpr_mov_b32 a13, a39
	v_accvgpr_write_b32 a20, v22
	v_mov_b32_dpp v11, v80 row_shl:1 row_mask:0xf bank_mask:0xf
	v_pk_fma_f32 v[60:61], v[80:81], v[122:123], v[60:61] op_sel_hi:[0,1,1]
	v_pk_mov_b32 v[62:63], v[80:81], v[100:101] op_sel:[1,0]
	v_mov_b32_dpp v2, v85 row_shr:1 row_mask:0xf bank_mask:0xf
	v_mov_b32_e32 v107, v85
	v_accvgpr_read_b32 v123, a11
	v_accvgpr_write_b32 a21, v23
	v_accvgpr_read_b32 v23, a13
	v_pk_fma_f32 v[60:61], v[62:63], v[10:11], v[60:61]
	v_pk_mul_f32 v[62:63], v[106:107], v[2:3]
	v_accvgpr_read_b32 v122, a10
	v_accvgpr_read_b32 v22, a12
	v_mov_b32_dpp v35, v84 row_shl:1 row_mask:0xf bank_mask:0xf
	v_pk_fma_f32 v[62:63], v[84:85], v[118:119], v[62:63] op_sel_hi:[0,1,1]
	v_accvgpr_write_b32 a12, v118
	v_pk_mov_b32 v[68:69], v[84:85], v[122:123] op_sel:[1,0]
	v_mov_b32_e32 v92, v59
	v_accvgpr_write_b32 a13, v119
	v_pk_fma_f32 v[62:63], v[68:69], v[34:35], v[62:63]
	v_pk_add_f32 v[60:61], v[60:61], 0 op_sel_hi:[1,0]
	v_mov_b32_dpp v92, v117 row_shr:1 row_mask:0xf bank_mask:0xf
	v_mov_b32_e32 v97, v117
	v_mov_b64_e32 v[118:119], v[40:41]
	v_accvgpr_read_b32 v40, a44
	v_pk_add_f32 v[60:61], v[60:61], v[62:63]
	v_pk_mul_f32 v[62:63], v[96:97], v[92:93]
	v_accvgpr_read_b32 v41, a45
	v_mov_b32_dpp v59, v116 row_shl:1 row_mask:0xf bank_mask:0xf
	v_pk_fma_f32 v[62:63], v[116:117], v[118:119], v[62:63] op_sel_hi:[0,1,1]
	v_pk_mov_b32 v[68:69], v[116:117], v[40:41] op_sel:[1,0]
	v_mov_b32_e32 v94, v57
	v_pk_fma_f32 v[62:63], v[68:69], v[58:59], v[62:63]
	s_mov_b64 s[0:1], 0x1020000
	v_pk_add_f32 v[60:61], v[60:61], v[62:63]
	v_mov_b32_dpp v94, v115 row_shr:1 row_mask:0xf bank_mask:0xf
	v_mov_b32_e32 v99, v115
	v_lshl_add_u64 v[62:63], v[54:55], 0, s[0:1]
	v_mov_b32_e32 v128, v60
	v_mov_b32_e32 v129, v61
	v_pk_mul_f32 v[60:61], v[98:99], v[94:95]
	v_mov_b32_e32 v102, v51
	v_accvgpr_write_b32 a30, v4
	v_mov_b32_dpp v57, v114 row_shl:1 row_mask:0xf bank_mask:0xf
	v_pk_fma_f32 v[60:61], v[114:115], v[14:15], v[60:61] op_sel_hi:[0,1,1]
	v_mov_b32_e32 v62, v115
	v_mov_b32_e32 v63, v101
	v_mov_b32_dpp v102, v113 row_shr:1 row_mask:0xf bank_mask:0xf
	v_mov_b32_e32 v105, v113
	v_accvgpr_read_b32 v4, a18
	v_pk_fma_f32 v[60:61], v[62:63], v[56:57], v[60:61]
	v_pk_mul_f32 v[62:63], v[104:105], v[102:103]
	v_accvgpr_read_b32 v5, a19
	v_mov_b32_dpp v51, v112 row_shl:1 row_mask:0xf bank_mask:0xf
	v_pk_fma_f32 v[62:63], v[112:113], v[4:5], v[62:63] op_sel_hi:[0,1,1]
	v_mov_b32_e32 v68, v113
	v_mov_b32_e32 v69, v123
	v_mov_b32_e32 v108, v49
	v_pk_fma_f32 v[62:63], v[68:69], v[50:51], v[62:63]
	v_pk_add_f32 v[60:61], v[60:61], 0 op_sel_hi:[1,0]
	v_mov_b32_dpp v108, v91 row_shr:1 row_mask:0xf bank_mask:0xf
	v_mov_b32_e32 v111, v91
	v_pk_add_f32 v[60:61], v[60:61], v[62:63]
	v_pk_mul_f32 v[62:63], v[110:111], v[108:109]
	v_mov_b32_dpp v49, v90 row_shl:1 row_mask:0xf bank_mask:0xf
	v_pk_fma_f32 v[62:63], v[90:91], v[8:9], v[62:63] op_sel_hi:[0,1,1]
	v_mov_b32_e32 v68, v91
	v_mov_b32_e32 v69, v41
	v_pk_fma_f32 v[62:63], v[68:69], v[48:49], v[62:63]
	s_mov_b64 s[0:1], 0x1030000
	v_pk_add_f32 v[60:61], v[60:61], v[62:63]
	v_lshl_add_u64 v[136:137], v[134:135], 0, s[0:1]
	s_nop 1
	s_mov_b64 vcc, s[28:29]
	s_nop 0
	v_cndmask_b32_dpp v130, v60, v128, vcc quad_perm:[1,0,3,2] row_mask:0xf bank_mask:0xf
	v_cndmask_b32_dpp v131, v61, v129, vcc quad_perm:[1,0,3,2] row_mask:0xf bank_mask:0xf
	s_mov_b64 vcc, s[30:31]
	s_nop 0
	v_cndmask_b32_dpp v132, v128, v60, vcc quad_perm:[1,0,3,2] row_mask:0xf bank_mask:0xf
	v_cndmask_b32_dpp v133, v129, v61, vcc quad_perm:[1,0,3,2] row_mask:0xf bank_mask:0xf
	global_store_dwordx4 v[136:137], v[130:133], off sc0 sc1 nt
	s_nop 1
	s_waitcnt vmcnt(16)
	s_waitcnt lgkmcnt(0)
	s_barrier
	v_accvgpr_read_b32 v2, a0
	v_accvgpr_read_b32 v8, a4
	ds_read_b64 v[60:61], v8
	ds_read_b64 v[62:63], v8 offset:288
	ds_read_b64 v[68:69], v8 offset:576
	ds_read_b64 v[70:71], v8 offset:1728
	ds_read_b64 v[72:73], v8 offset:2016
	ds_read_b64 v[82:83], v8 offset:2304
	ds_read_b64 v[80:81], v8 offset:3456
	ds_read_b64 v[84:85], v8 offset:3744
	ds_read_b64 v[116:117], v8 offset:4032
	ds_read_b64 v[114:115], v8 offset:5184
	ds_read_b64 v[112:113], v8 offset:5472
	ds_read_b64 v[90:91], v8 offset:5760
	ds_read_b32 v43, v2
	ds_read_b32 v19, v2 offset:288
	ds_read_b32 v39, v2 offset:576
	ds_read_b32 v25, v2 offset:1728
	ds_read_b32 v7, v2 offset:2016
	ds_read_b32 v21, v2 offset:2304
	ds_read_b32 v11, v2 offset:3456
	ds_read_b32 v35, v2 offset:3744
	ds_read_b32 v59, v2 offset:4032
	ds_read_b32 v57, v2 offset:5184
	ds_read_b32 v51, v2 offset:5472
	ds_read_b32 v49, v2 offset:5760
	s_waitcnt lgkmcnt(0)
	v_mov_b32_e32 v64, v32
	v_mov_b32_e32 v46, v43
	v_mov_b32_e32 v65, v61
	v_mov_b64_e32 v[100:101], v[22:23]
	v_mov_b32_dpp v46, v61 row_shr:1 row_mask:0xf bank_mask:0xf
	v_pk_mul_f32 v[86:87], v[64:65], v[46:47]
	v_mov_b32_e32 v26, v19
	v_mov_b32_dpp v43, v60 row_shl:1 row_mask:0xf bank_mask:0xf
	v_pk_fma_f32 v[86:87], v[60:61], v[88:89], v[86:87] op_sel_hi:[0,1,1]
	v_pk_mov_b32 v[60:61], v[60:61], v[100:101] op_sel:[1,0]
	v_mov_b32_dpp v26, v63 row_shr:1 row_mask:0xf bank_mask:0xf
	v_mov_b32_e32 v1, v63
	v_accvgpr_read_b32 v67, a35
	v_pk_fma_f32 v[60:61], v[60:61], v[42:43], v[86:87]
	v_pk_mul_f32 v[86:87], v[0:1], v[26:27]
	v_accvgpr_read_b32 v66, a34
	v_accvgpr_write_b32 a10, v14
	v_mov_b32_dpp v19, v62 row_shl:1 row_mask:0xf bank_mask:0xf
	v_pk_fma_f32 v[86:87], v[62:63], v[16:17], v[86:87] op_sel_hi:[0,1,1]
	v_pk_mov_b32 v[62:63], v[62:63], v[66:67] op_sel:[1,0]
	v_mov_b32_e32 v44, v39
	v_accvgpr_write_b32 a11, v15
	v_pk_fma_f32 v[62:63], v[62:63], v[18:19], v[86:87]
	v_pk_add_f32 v[60:61], v[60:61], 0 op_sel_hi:[1,0]
	v_mov_b32_dpp v44, v69 row_shr:1 row_mask:0xf bank_mask:0xf
	v_mov_b32_e32 v31, v69
	v_accvgpr_read_b32 v14, a16
	v_accvgpr_read_b32 v28, a46
	v_pk_add_f32 v[60:61], v[60:61], v[62:63]
	v_pk_mul_f32 v[62:63], v[30:31], v[44:45]
	v_accvgpr_read_b32 v15, a17
	v_accvgpr_read_b32 v29, a47
	v_mov_b32_dpp v39, v68 row_shl:1 row_mask:0xf bank_mask:0xf
	v_pk_fma_f32 v[62:63], v[68:69], v[14:15], v[62:63] op_sel_hi:[0,1,1]
	v_pk_mov_b32 v[68:69], v[68:69], v[28:29] op_sel:[1,0]
	v_mov_b32_e32 v36, v25
	v_pk_fma_f32 v[62:63], v[68:69], v[38:39], v[62:63]
	s_mov_b64 s[0:1], 0x1400000
	v_pk_add_f32 v[60:61], v[60:61], v[62:63]
	v_mov_b32_dpp v36, v71 row_shr:1 row_mask:0xf bank_mask:0xf
	v_mov_b32_e32 v127, v71
	v_accvgpr_read_b32 v8, a20
	v_lshl_add_u64 v[62:63], v[54:55], 0, s[0:1]
	v_mov_b32_e32 v128, v60
	v_mov_b32_e32 v129, v61
	v_pk_mul_f32 v[60:61], v[126:127], v[36:37]
	v_accvgpr_read_b32 v9, a21
	v_accvgpr_write_b32 a25, v23
	v_mov_b32_e32 v12, v7
	v_mov_b32_dpp v25, v70 row_shl:1 row_mask:0xf bank_mask:0xf
	v_pk_fma_f32 v[60:61], v[70:71], v[8:9], v[60:61] op_sel_hi:[0,1,1]
	v_mov_b32_e32 v62, v71
	v_mov_b32_e32 v63, v101
	v_accvgpr_write_b32 a24, v22
	v_mov_b32_dpp v12, v73 row_shr:1 row_mask:0xf bank_mask:0xf
	v_mov_b32_e32 v74, v52
	v_mov_b32_e32 v75, v73
	v_accvgpr_read_b32 v23, a9
	v_accvgpr_write_b32 a26, v124
	v_accvgpr_mov_b32 a2, a22
	v_pk_fma_f32 v[60:61], v[62:63], v[24:25], v[60:61]
	v_pk_mul_f32 v[62:63], v[74:75], v[12:13]
	v_accvgpr_read_b32 v22, a8
	v_accvgpr_write_b32 a27, v125
	v_accvgpr_mov_b32 a3, a23
	v_accvgpr_write_b32 a22, v88
	v_mov_b32_dpp v7, v72 row_shl:1 row_mask:0xf bank_mask:0xf
	v_pk_fma_f32 v[62:63], v[72:73], v[22:23], v[62:63] op_sel_hi:[0,1,1]
	v_mov_b32_e32 v68, v73
	v_mov_b32_e32 v69, v67
	v_mov_b32_e32 v78, v21
	v_accvgpr_write_b32 a23, v89
	v_pk_fma_f32 v[62:63], v[68:69], v[6:7], v[62:63]
	v_pk_add_f32 v[60:61], v[60:61], 0 op_sel_hi:[1,0]
	v_mov_b32_dpp v78, v83 row_shr:1 row_mask:0xf bank_mask:0xf
	v_accvgpr_read_b32 v52, a30
	v_mov_b32_e32 v53, v83
	v_accvgpr_read_b32 v89, a27
	v_pk_add_f32 v[60:61], v[60:61], v[62:63]
	v_pk_mul_f32 v[62:63], v[52:53], v[78:79]
	v_accvgpr_read_b32 v88, a26
	v_mov_b32_dpp v21, v82 row_shl:1 row_mask:0xf bank_mask:0xf
	v_pk_fma_f32 v[62:63], v[82:83], v[88:89], v[62:63] op_sel_hi:[0,1,1]
	v_mov_b32_e32 v68, v83
	v_mov_b32_e32 v69, v29
	v_pk_fma_f32 v[62:63], v[68:69], v[20:21], v[62:63]
	v_mov_b32_e32 v76, v11
	v_accvgpr_read_b32 v125, a37
	v_pk_add_f32 v[60:61], v[60:61], v[62:63]
	s_mov_b64 s[0:1], 0x1410000
	v_mov_b32_dpp v76, v81 row_shr:1 row_mask:0xf bank_mask:0xf
	v_mov_b32_e32 v121, v81
	v_accvgpr_read_b32 v101, a15
	v_accvgpr_read_b32 v124, a36
	v_lshl_add_u64 v[136:137], v[134:135], 0, s[0:1]
	s_nop 1
	s_mov_b64 vcc, s[28:29]
	s_nop 0
	v_cndmask_b32_dpp v130, v60, v128, vcc quad_perm:[1,0,3,2] row_mask:0xf bank_mask:0xf
	v_cndmask_b32_dpp v131, v61, v129, vcc quad_perm:[1,0,3,2] row_mask:0xf bank_mask:0xf
	s_mov_b64 vcc, s[30:31]
	s_nop 0
	v_cndmask_b32_dpp v132, v128, v60, vcc quad_perm:[1,0,3,2] row_mask:0xf bank_mask:0xf
	v_cndmask_b32_dpp v133, v129, v61, vcc quad_perm:[1,0,3,2] row_mask:0xf bank_mask:0xf
	global_store_dwordx4 v[136:137], v[130:133], off sc0 sc1 nt
	s_nop 1
	v_pk_mul_f32 v[60:61], v[120:121], v[76:77]
	v_accvgpr_read_b32 v100, a14
	v_mov_b32_e32 v2, v35
	v_mov_b32_dpp v11, v80 row_shl:1 row_mask:0xf bank_mask:0xf
	v_pk_fma_f32 v[60:61], v[80:81], v[124:125], v[60:61] op_sel_hi:[0,1,1]
	v_pk_mov_b32 v[62:63], v[80:81], v[100:101] op_sel:[1,0]
	v_mov_b32_dpp v2, v85 row_shr:1 row_mask:0xf bank_mask:0xf
	v_mov_b32_e32 v107, v85
	v_accvgpr_read_b32 v29, a13
	v_pk_fma_f32 v[60:61], v[62:63], v[10:11], v[60:61]
	v_pk_mul_f32 v[62:63], v[106:107], v[2:3]
	v_accvgpr_read_b32 v28, a12
	v_mov_b32_dpp v35, v84 row_shl:1 row_mask:0xf bank_mask:0xf
	v_pk_fma_f32 v[62:63], v[84:85], v[28:29], v[62:63] op_sel_hi:[0,1,1]
	v_pk_mov_b32 v[68:69], v[84:85], v[122:123] op_sel:[1,0]
	v_mov_b32_e32 v92, v59
	v_pk_fma_f32 v[62:63], v[68:69], v[34:35], v[62:63]
	v_pk_add_f32 v[60:61], v[60:61], 0 op_sel_hi:[1,0]
	v_mov_b32_dpp v92, v117 row_shr:1 row_mask:0xf bank_mask:0xf
	v_mov_b32_e32 v97, v117
	v_pk_add_f32 v[60:61], v[60:61], v[62:63]
	v_pk_mul_f32 v[62:63], v[96:97], v[92:93]
	v_accvgpr_write_b32 a8, v118
	v_pk_fma_f32 v[62:63], v[116:117], v[118:119], v[62:63] op_sel_hi:[0,1,1]
	v_accvgpr_write_b32 a9, v119
	v_accvgpr_read_b32 v119, a45
	v_accvgpr_read_b32 v118, a44
	v_mov_b32_dpp v59, v116 row_shl:1 row_mask:0xf bank_mask:0xf
	v_pk_mov_b32 v[68:69], v[116:117], v[118:119] op_sel:[1,0]
	v_mov_b32_e32 v94, v57
	v_pk_fma_f32 v[62:63], v[68:69], v[58:59], v[62:63]
	s_mov_b64 s[0:1], 0x1420000
	v_pk_add_f32 v[60:61], v[60:61], v[62:63]
	v_mov_b32_dpp v94, v115 row_shr:1 row_mask:0xf bank_mask:0xf
	v_mov_b32_e32 v99, v115
	v_accvgpr_read_b32 v41, a11
	v_lshl_add_u64 v[62:63], v[54:55], 0, s[0:1]
	v_mov_b32_e32 v128, v60
	v_mov_b32_e32 v129, v61
	v_pk_mul_f32 v[60:61], v[98:99], v[94:95]
	v_accvgpr_read_b32 v40, a10
	v_mov_b32_e32 v102, v51
	v_mov_b32_dpp v57, v114 row_shl:1 row_mask:0xf bank_mask:0xf
	v_pk_fma_f32 v[60:61], v[114:115], v[40:41], v[60:61] op_sel_hi:[0,1,1]
	v_mov_b32_e32 v62, v115
	v_mov_b32_e32 v63, v101
	v_mov_b32_dpp v102, v113 row_shr:1 row_mask:0xf bank_mask:0xf
	v_mov_b32_e32 v105, v113
	v_pk_fma_f32 v[60:61], v[62:63], v[56:57], v[60:61]
	v_pk_mul_f32 v[62:63], v[104:105], v[102:103]
	v_mov_b32_dpp v51, v112 row_shl:1 row_mask:0xf bank_mask:0xf
	v_pk_fma_f32 v[62:63], v[112:113], v[4:5], v[62:63] op_sel_hi:[0,1,1]
	v_mov_b32_e32 v68, v113
	v_mov_b32_e32 v69, v123
	v_mov_b32_e32 v108, v49
	v_pk_fma_f32 v[62:63], v[68:69], v[50:51], v[62:63]
	v_pk_add_f32 v[60:61], v[60:61], 0 op_sel_hi:[1,0]
	v_mov_b32_dpp v108, v91 row_shr:1 row_mask:0xf bank_mask:0xf
	v_mov_b32_e32 v111, v91
	v_accvgpr_read_b32 v5, a3
	v_pk_add_f32 v[60:61], v[60:61], v[62:63]
	v_pk_mul_f32 v[62:63], v[110:111], v[108:109]
	v_accvgpr_read_b32 v4, a2
	v_mov_b32_dpp v49, v90 row_shl:1 row_mask:0xf bank_mask:0xf
	v_pk_fma_f32 v[62:63], v[90:91], v[4:5], v[62:63] op_sel_hi:[0,1,1]
	v_mov_b32_e32 v68, v91
	v_mov_b32_e32 v69, v119
	v_pk_fma_f32 v[62:63], v[68:69], v[48:49], v[62:63]
	s_mov_b64 s[0:1], 0x1430000
	v_pk_add_f32 v[60:61], v[60:61], v[62:63]
	v_lshl_add_u64 v[136:137], v[134:135], 0, s[0:1]
	s_nop 1
	s_mov_b64 vcc, s[28:29]
	s_nop 0
	v_cndmask_b32_dpp v130, v60, v128, vcc quad_perm:[1,0,3,2] row_mask:0xf bank_mask:0xf
	v_cndmask_b32_dpp v131, v61, v129, vcc quad_perm:[1,0,3,2] row_mask:0xf bank_mask:0xf
	s_mov_b64 vcc, s[30:31]
	s_nop 0
	v_cndmask_b32_dpp v132, v128, v60, vcc quad_perm:[1,0,3,2] row_mask:0xf bank_mask:0xf
	v_cndmask_b32_dpp v133, v129, v61, vcc quad_perm:[1,0,3,2] row_mask:0xf bank_mask:0xf
	global_store_dwordx4 v[136:137], v[130:133], off sc0 sc1 nt
	s_nop 1
	s_waitcnt vmcnt(12)
	s_waitcnt lgkmcnt(0)
	s_barrier
	v_accvgpr_read_b32 v2, a1
	v_accvgpr_read_b32 v12, a5
	ds_read_b64 v[60:61], v12
	ds_read_b64 v[62:63], v12 offset:288
	ds_read_b64 v[68:69], v12 offset:576
	ds_read_b64 v[70:71], v12 offset:1728
	ds_read_b64 v[72:73], v12 offset:2016
	ds_read_b64 v[82:83], v12 offset:2304
	ds_read_b64 v[80:81], v12 offset:3456
	ds_read_b64 v[84:85], v12 offset:3744
	ds_read_b64 v[116:117], v12 offset:4032
	ds_read_b64 v[114:115], v12 offset:5184
	ds_read_b64 v[112:113], v12 offset:5472
	ds_read_b64 v[90:91], v12 offset:5760
	ds_read_b32 v43, v2
	ds_read_b32 v19, v2 offset:288
	ds_read_b32 v39, v2 offset:576
	ds_read_b32 v25, v2 offset:1728
	ds_read_b32 v7, v2 offset:2016
	ds_read_b32 v21, v2 offset:2304
	ds_read_b32 v11, v2 offset:3456
	ds_read_b32 v35, v2 offset:3744
	ds_read_b32 v59, v2 offset:4032
	ds_read_b32 v57, v2 offset:5184
	ds_read_b32 v51, v2 offset:5472
	ds_read_b32 v49, v2 offset:5760
	s_waitcnt lgkmcnt(0)
	v_accvgpr_read_b32 v101, a23
	v_mov_b32_e32 v46, v43
	v_mov_b32_e32 v65, v61
	v_accvgpr_read_b32 v31, a25
	v_mov_b32_dpp v46, v61 row_shr:1 row_mask:0xf bank_mask:0xf
	v_pk_mul_f32 v[86:87], v[64:65], v[46:47]
	v_accvgpr_read_b32 v100, a22
	v_accvgpr_read_b32 v30, a24
	v_mov_b32_e32 v26, v19
	v_mov_b32_dpp v43, v60 row_shl:1 row_mask:0xf bank_mask:0xf
	v_pk_fma_f32 v[86:87], v[60:61], v[100:101], v[86:87] op_sel_hi:[0,1,1]
	v_pk_mov_b32 v[60:61], v[60:61], v[30:31] op_sel:[1,0]
	v_mov_b32_dpp v26, v63 row_shr:1 row_mask:0xf bank_mask:0xf
	v_mov_b32_e32 v1, v63
	v_pk_fma_f32 v[60:61], v[60:61], v[42:43], v[86:87]
	v_pk_mul_f32 v[86:87], v[0:1], v[26:27]
	v_accvgpr_read_b32 v0, a34
	v_accvgpr_mov_b32 a12, a14
	v_accvgpr_read_b32 v1, a35
	v_accvgpr_mov_b32 a13, a15
	v_mov_b32_dpp v19, v62 row_shl:1 row_mask:0xf bank_mask:0xf
	v_pk_fma_f32 v[86:87], v[62:63], v[16:17], v[86:87] op_sel_hi:[0,1,1]
	v_accvgpr_write_b32 a14, v16
	v_pk_mov_b32 v[62:63], v[62:63], v[0:1] op_sel:[1,0]
	v_mov_b32_e32 v44, v39
	v_accvgpr_write_b32 a15, v17
	v_pk_fma_f32 v[62:63], v[62:63], v[18:19], v[86:87]
	v_pk_add_f32 v[60:61], v[60:61], 0 op_sel_hi:[1,0]
	v_mov_b32_dpp v44, v69 row_shr:1 row_mask:0xf bank_mask:0xf
	v_accvgpr_read_b32 v16, a48
	v_mov_b32_e32 v17, v69
	v_accvgpr_read_b32 v67, a47
	v_pk_add_f32 v[60:61], v[60:61], v[62:63]
	v_pk_mul_f32 v[62:63], v[16:17], v[44:45]
	v_accvgpr_read_b32 v66, a46
	v_mov_b32_dpp v39, v68 row_shl:1 row_mask:0xf bank_mask:0xf
	v_pk_fma_f32 v[62:63], v[68:69], v[14:15], v[62:63] op_sel_hi:[0,1,1]
	v_pk_mov_b32 v[68:69], v[68:69], v[66:67] op_sel:[1,0]
	v_mov_b32_e32 v36, v25
	v_pk_fma_f32 v[62:63], v[68:69], v[38:39], v[62:63]
	s_mov_b64 s[0:1], 0x1800000
	v_pk_add_f32 v[60:61], v[60:61], v[62:63]
	v_mov_b32_dpp v36, v71 row_shr:1 row_mask:0xf bank_mask:0xf
	v_mov_b32_e32 v127, v71
	v_lshl_add_u64 v[62:63], v[54:55], 0, s[0:1]
	v_mov_b32_e32 v128, v60
	v_mov_b32_e32 v129, v61
	v_pk_mul_f32 v[60:61], v[126:127], v[36:37]
	v_mov_b32_e32 v12, v7
	v_mov_b32_dpp v25, v70 row_shl:1 row_mask:0xf bank_mask:0xf
	v_pk_fma_f32 v[60:61], v[70:71], v[8:9], v[60:61] op_sel_hi:[0,1,1]
	v_mov_b32_e32 v62, v71
	v_mov_b32_e32 v63, v31
	v_mov_b32_dpp v12, v73 row_shr:1 row_mask:0xf bank_mask:0xf
	v_mov_b32_e32 v75, v73
	v_pk_fma_f32 v[60:61], v[62:63], v[24:25], v[60:61]
	v_pk_mul_f32 v[62:63], v[74:75], v[12:13]
	v_mov_b32_dpp v7, v72 row_shl:1 row_mask:0xf bank_mask:0xf
	v_pk_fma_f32 v[62:63], v[72:73], v[22:23], v[62:63] op_sel_hi:[0,1,1]
	v_accvgpr_write_b32 a4, v22
	v_mov_b32_e32 v68, v73
	v_mov_b32_e32 v69, v1
	v_mov_b32_e32 v78, v21
	v_accvgpr_write_b32 a5, v23
	v_pk_fma_f32 v[62:63], v[68:69], v[6:7], v[62:63]
	v_pk_add_f32 v[60:61], v[60:61], 0 op_sel_hi:[1,0]
	v_mov_b32_dpp v78, v83 row_shr:1 row_mask:0xf bank_mask:0xf
	v_mov_b32_e32 v53, v83
	v_accvgpr_read_b32 v22, a26
	v_pk_add_f32 v[60:61], v[60:61], v[62:63]
	v_pk_mul_f32 v[62:63], v[52:53], v[78:79]
	v_accvgpr_read_b32 v23, a27
	v_mov_b32_dpp v21, v82 row_shl:1 row_mask:0xf bank_mask:0xf
	v_pk_fma_f32 v[62:63], v[82:83], v[22:23], v[62:63] op_sel_hi:[0,1,1]
	v_mov_b32_e32 v68, v83
	v_mov_b32_e32 v69, v67
	v_pk_fma_f32 v[62:63], v[68:69], v[20:21], v[62:63]
	v_mov_b32_e32 v76, v11
	v_pk_add_f32 v[60:61], v[60:61], v[62:63]
	s_mov_b64 s[0:1], 0x1810000
	v_mov_b32_dpp v76, v81 row_shr:1 row_mask:0xf bank_mask:0xf
	v_mov_b32_e32 v121, v81
	v_accvgpr_read_b32 v15, a13
	v_lshl_add_u64 v[136:137], v[134:135], 0, s[0:1]
	s_nop 1
	s_mov_b64 vcc, s[28:29]
	s_nop 0
	v_cndmask_b32_dpp v130, v60, v128, vcc quad_perm:[1,0,3,2] row_mask:0xf bank_mask:0xf
	v_cndmask_b32_dpp v131, v61, v129, vcc quad_perm:[1,0,3,2] row_mask:0xf bank_mask:0xf
	s_mov_b64 vcc, s[30:31]
	s_nop 0
	v_cndmask_b32_dpp v132, v128, v60, vcc quad_perm:[1,0,3,2] row_mask:0xf bank_mask:0xf
	v_cndmask_b32_dpp v133, v129, v61, vcc quad_perm:[1,0,3,2] row_mask:0xf bank_mask:0xf
	global_store_dwordx4 v[136:137], v[130:133], off sc0 sc1 nt
	s_nop 1
	v_pk_mul_f32 v[60:61], v[120:121], v[76:77]
	v_accvgpr_read_b32 v14, a12
	v_mov_b32_e32 v2, v35
	v_mov_b32_dpp v11, v80 row_shl:1 row_mask:0xf bank_mask:0xf
	v_pk_fma_f32 v[60:61], v[80:81], v[124:125], v[60:61] op_sel_hi:[0,1,1]
	v_pk_mov_b32 v[62:63], v[80:81], v[14:15] op_sel:[1,0]
	v_mov_b32_dpp v2, v85 row_shr:1 row_mask:0xf bank_mask:0xf
	v_mov_b32_e32 v107, v85
	v_pk_fma_f32 v[60:61], v[62:63], v[10:11], v[60:61]
	v_pk_mul_f32 v[62:63], v[106:107], v[2:3]
	v_mov_b32_dpp v35, v84 row_shl:1 row_mask:0xf bank_mask:0xf
	v_pk_fma_f32 v[62:63], v[84:85], v[28:29], v[62:63] op_sel_hi:[0,1,1]
	v_pk_mov_b32 v[68:69], v[84:85], v[122:123] op_sel:[1,0]
	v_mov_b32_e32 v92, v59
	v_pk_fma_f32 v[62:63], v[68:69], v[34:35], v[62:63]
	v_pk_add_f32 v[60:61], v[60:61], 0 op_sel_hi:[1,0]
	v_mov_b32_dpp v92, v117 row_shr:1 row_mask:0xf bank_mask:0xf
	v_mov_b32_e32 v97, v117
	v_accvgpr_read_b32 v87, a9
	v_pk_add_f32 v[60:61], v[60:61], v[62:63]
	v_pk_mul_f32 v[62:63], v[96:97], v[92:93]
	v_accvgpr_read_b32 v86, a8
	v_mov_b32_dpp v59, v116 row_shl:1 row_mask:0xf bank_mask:0xf
	v_pk_fma_f32 v[62:63], v[116:117], v[86:87], v[62:63] op_sel_hi:[0,1,1]
	v_pk_mov_b32 v[68:69], v[116:117], v[118:119] op_sel:[1,0]
	v_mov_b32_e32 v94, v57
	v_pk_fma_f32 v[62:63], v[68:69], v[58:59], v[62:63]
	s_mov_b64 s[0:1], 0x1820000
	v_pk_add_f32 v[60:61], v[60:61], v[62:63]
	v_mov_b32_dpp v94, v115 row_shr:1 row_mask:0xf bank_mask:0xf
	v_mov_b32_e32 v99, v115
	v_lshl_add_u64 v[62:63], v[54:55], 0, s[0:1]
	v_mov_b32_e32 v128, v60
	v_mov_b32_e32 v129, v61
	v_pk_mul_f32 v[60:61], v[98:99], v[94:95]
	v_mov_b32_e32 v102, v51
	v_mov_b32_dpp v57, v114 row_shl:1 row_mask:0xf bank_mask:0xf
	v_pk_fma_f32 v[60:61], v[114:115], v[40:41], v[60:61] op_sel_hi:[0,1,1]
	v_mov_b32_e32 v62, v115
	v_mov_b32_e32 v63, v15
	v_mov_b32_dpp v102, v113 row_shr:1 row_mask:0xf bank_mask:0xf
	v_mov_b32_e32 v105, v113
	v_accvgpr_read_b32 v89, a19
	v_pk_fma_f32 v[60:61], v[62:63], v[56:57], v[60:61]
	v_pk_mul_f32 v[62:63], v[104:105], v[102:103]
	v_accvgpr_read_b32 v88, a18
	v_mov_b32_dpp v51, v112 row_shl:1 row_mask:0xf bank_mask:0xf
	v_pk_fma_f32 v[62:63], v[112:113], v[88:89], v[62:63] op_sel_hi:[0,1,1]
	v_mov_b32_e32 v68, v113
	v_mov_b32_e32 v69, v123
	v_mov_b32_e32 v108, v49
	v_pk_fma_f32 v[62:63], v[68:69], v[50:51], v[62:63]
	v_pk_add_f32 v[60:61], v[60:61], 0 op_sel_hi:[1,0]
	v_mov_b32_dpp v108, v91 row_shr:1 row_mask:0xf bank_mask:0xf
	v_mov_b32_e32 v111, v91
	v_pk_add_f32 v[60:61], v[60:61], v[62:63]
	v_pk_mul_f32 v[62:63], v[110:111], v[108:109]
	v_mov_b32_dpp v49, v90 row_shl:1 row_mask:0xf bank_mask:0xf
	v_pk_fma_f32 v[62:63], v[90:91], v[4:5], v[62:63] op_sel_hi:[0,1,1]
	v_mov_b32_e32 v68, v91
	v_mov_b32_e32 v69, v119
	v_pk_fma_f32 v[62:63], v[68:69], v[48:49], v[62:63]
	s_mov_b64 s[0:1], 0x1830000
	v_pk_add_f32 v[60:61], v[60:61], v[62:63]
	v_lshl_add_u64 v[136:137], v[134:135], 0, s[0:1]
	s_nop 1
	s_mov_b64 vcc, s[28:29]
	s_nop 0
	v_cndmask_b32_dpp v130, v60, v128, vcc quad_perm:[1,0,3,2] row_mask:0xf bank_mask:0xf
	v_cndmask_b32_dpp v131, v61, v129, vcc quad_perm:[1,0,3,2] row_mask:0xf bank_mask:0xf
	s_mov_b64 vcc, s[30:31]
	s_nop 0
	v_cndmask_b32_dpp v132, v128, v60, vcc quad_perm:[1,0,3,2] row_mask:0xf bank_mask:0xf
	v_cndmask_b32_dpp v133, v129, v61, vcc quad_perm:[1,0,3,2] row_mask:0xf bank_mask:0xf
	global_store_dwordx4 v[136:137], v[130:133], off sc0 sc1 nt
	s_nop 1
	v_accvgpr_write_b32 a12, v28
	s_waitcnt vmcnt(8)
	v_accvgpr_write_b32 a13, v29
	v_mov_b64_e32 v[28:29], v[4:5]
	s_waitcnt lgkmcnt(0)
	s_barrier
	v_accvgpr_read_b32 v2, a6
	v_accvgpr_read_b32 v4, a7
	ds_read_b64 v[60:61], v2
	ds_read_b64 v[62:63], v2 offset:288
	ds_read_b64 v[68:69], v2 offset:576
	ds_read_b64 v[70:71], v2 offset:1728
	ds_read_b64 v[72:73], v2 offset:2016
	ds_read_b64 v[82:83], v2 offset:2304
	ds_read_b64 v[80:81], v2 offset:3456
	ds_read_b64 v[84:85], v2 offset:3744
	ds_read_b64 v[116:117], v2 offset:4032
	ds_read_b64 v[114:115], v2 offset:5184
	ds_read_b64 v[112:113], v2 offset:5472
	ds_read_b64 v[90:91], v2 offset:5760
	ds_read_b32 v43, v4
	ds_read_b32 v19, v4 offset:288
	ds_read_b32 v39, v4 offset:576
	ds_read_b32 v25, v4 offset:1728
	ds_read_b32 v7, v4 offset:2016
	ds_read_b32 v21, v4 offset:2304
	ds_read_b32 v11, v4 offset:3456
	ds_read_b32 v35, v4 offset:3744
	ds_read_b32 v59, v4 offset:4032
	ds_read_b32 v57, v4 offset:5184
	ds_read_b32 v51, v4 offset:5472
	ds_read_b32 v49, v4 offset:5760
	s_waitcnt lgkmcnt(0)
	v_accvgpr_read_b32 v8, a24
	v_mov_b32_e32 v46, v43
	v_mov_b32_e32 v65, v61
	v_mov_b32_e32 v26, v19
	v_mov_b32_dpp v46, v61 row_shr:1 row_mask:0xf bank_mask:0xf
	v_accvgpr_read_b32 v32, a32
	v_accvgpr_read_b32 v9, a25
	v_mov_b64_e32 v[124:125], v[40:41]
	v_pk_mul_f32 v[30:31], v[64:65], v[46:47]
	v_mov_b32_dpp v26, v63 row_shr:1 row_mask:0xf bank_mask:0xf
	v_mov_b32_e32 v33, v63
	v_accvgpr_read_b32 v4, a14
	v_accvgpr_read_b32 v41, a35
	v_mov_b32_e32 v44, v39
	v_pk_fma_f32 v[30:31], v[60:61], v[100:101], v[30:31] op_sel_hi:[0,1,1]
	v_mov_b32_dpp v43, v60 row_shl:1 row_mask:0xf bank_mask:0xf
	v_pk_mov_b32 v[46:47], v[60:61], v[8:9] op_sel:[1,0]
	v_pk_mul_f32 v[26:27], v[32:33], v[26:27]
	v_accvgpr_read_b32 v5, a15
	v_accvgpr_read_b32 v40, a34
	v_mov_b32_dpp v44, v69 row_shr:1 row_mask:0xf bank_mask:0xf
	v_mov_b32_e32 v17, v69
	v_accvgpr_read_b32 v0, a16
	v_pk_fma_f32 v[30:31], v[46:47], v[42:43], v[30:31]
	v_pk_fma_f32 v[26:27], v[62:63], v[4:5], v[26:27] op_sel_hi:[0,1,1]
	v_mov_b32_dpp v19, v62 row_shl:1 row_mask:0xf bank_mask:0xf
	v_pk_mov_b32 v[32:33], v[62:63], v[40:41] op_sel:[1,0]
	v_pk_mul_f32 v[16:17], v[16:17], v[44:45]
	v_accvgpr_read_b32 v1, a17
	v_pk_fma_f32 v[18:19], v[32:33], v[18:19], v[26:27]
	v_pk_add_f32 v[26:27], v[30:31], 0 op_sel_hi:[1,0]
	v_mov_b32_dpp v39, v68 row_shl:1 row_mask:0xf bank_mask:0xf
	v_pk_fma_f32 v[16:17], v[68:69], v[0:1], v[16:17] op_sel_hi:[0,1,1]
	v_pk_mov_b32 v[30:31], v[68:69], v[66:67] op_sel:[1,0]
	v_pk_add_f32 v[18:19], v[26:27], v[18:19]
	v_pk_fma_f32 v[16:17], v[30:31], v[38:39], v[16:17]
	v_mov_b32_e32 v36, v25
	s_mov_b64 s[0:1], 0x1c00000
	v_pk_add_f32 v[16:17], v[18:19], v[16:17]
	v_mov_b32_dpp v36, v71 row_shr:1 row_mask:0xf bank_mask:0xf
	v_mov_b32_e32 v127, v71
	v_accvgpr_read_b32 v0, a20
	v_lshl_add_u64 v[26:27], v[54:55], 0, s[0:1]
	v_mov_b32_e32 v128, v16
	v_mov_b32_e32 v129, v17
	v_mov_b32_e32 v12, v7
	v_pk_mul_f32 v[16:17], v[126:127], v[36:37]
	v_accvgpr_read_b32 v1, a21
	v_mov_b32_dpp v12, v73 row_shr:1 row_mask:0xf bank_mask:0xf
	v_pk_fma_f32 v[16:17], v[70:71], v[0:1], v[16:17] op_sel_hi:[0,1,1]
	v_mov_b32_e32 v75, v73
	v_accvgpr_read_b32 v0, a4
	v_mov_b32_e32 v78, v21
	v_pk_mul_f32 v[12:13], v[74:75], v[12:13]
	v_accvgpr_read_b32 v1, a5
	v_mov_b32_dpp v25, v70 row_shl:1 row_mask:0xf bank_mask:0xf
	v_mov_b32_dpp v7, v72 row_shl:1 row_mask:0xf bank_mask:0xf
	v_mov_b32_dpp v78, v83 row_shr:1 row_mask:0xf bank_mask:0xf
	v_mov_b32_e32 v8, v71
	v_pk_fma_f32 v[12:13], v[72:73], v[0:1], v[12:13] op_sel_hi:[0,1,1]
	v_mov_b32_e32 v5, v41
	v_mov_b32_e32 v4, v73
	v_mov_b32_e32 v53, v83
	v_pk_fma_f32 v[16:17], v[8:9], v[24:25], v[16:17]
	v_pk_fma_f32 v[6:7], v[4:5], v[6:7], v[12:13]
	v_pk_mul_f32 v[12:13], v[52:53], v[78:79]
	v_mov_b32_dpp v21, v82 row_shl:1 row_mask:0xf bank_mask:0xf
	v_pk_add_f32 v[16:17], v[16:17], 0 op_sel_hi:[1,0]
	v_pk_fma_f32 v[12:13], v[82:83], v[22:23], v[12:13] op_sel_hi:[0,1,1]
	v_mov_b32_e32 v66, v83
	v_pk_add_f32 v[6:7], v[16:17], v[6:7]
	v_pk_fma_f32 v[12:13], v[66:67], v[20:21], v[12:13]
	v_mov_b32_e32 v76, v11
	v_pk_add_f32 v[6:7], v[6:7], v[12:13]
	s_mov_b64 s[0:1], 0x1c10000
	v_mov_b32_dpp v76, v81 row_shr:1 row_mask:0xf bank_mask:0xf
	v_mov_b32_e32 v121, v81
	v_accvgpr_read_b32 v0, a36
	v_lshl_add_u64 v[136:137], v[134:135], 0, s[0:1]
	s_nop 1
	s_mov_b64 vcc, s[28:29]
	s_nop 0
	v_cndmask_b32_dpp v130, v6, v128, vcc quad_perm:[1,0,3,2] row_mask:0xf bank_mask:0xf
	v_cndmask_b32_dpp v131, v7, v129, vcc quad_perm:[1,0,3,2] row_mask:0xf bank_mask:0xf
	s_mov_b64 vcc, s[30:31]
	s_nop 0
	v_cndmask_b32_dpp v132, v128, v6, vcc quad_perm:[1,0,3,2] row_mask:0xf bank_mask:0xf
	v_cndmask_b32_dpp v133, v129, v7, vcc quad_perm:[1,0,3,2] row_mask:0xf bank_mask:0xf
	global_store_dwordx4 v[136:137], v[130:133], off sc0 sc1 nt
	s_nop 1
	v_mov_b32_e32 v2, v35
	v_pk_mul_f32 v[6:7], v[120:121], v[76:77]
	v_accvgpr_read_b32 v1, a37
	v_mov_b32_dpp v2, v85 row_shr:1 row_mask:0xf bank_mask:0xf
	v_pk_fma_f32 v[6:7], v[80:81], v[0:1], v[6:7] op_sel_hi:[0,1,1]
	v_mov_b32_e32 v107, v85
	v_accvgpr_read_b32 v0, a12
	v_mov_b32_e32 v92, v59
	v_pk_mul_f32 v[2:3], v[106:107], v[2:3]
	v_accvgpr_read_b32 v1, a13
	v_mov_b32_dpp v11, v80 row_shl:1 row_mask:0xf bank_mask:0xf
	v_mov_b32_dpp v35, v84 row_shl:1 row_mask:0xf bank_mask:0xf
	v_mov_b32_dpp v92, v117 row_shr:1 row_mask:0xf bank_mask:0xf
	v_pk_mov_b32 v[8:9], v[80:81], v[14:15] op_sel:[1,0]
	v_pk_fma_f32 v[2:3], v[84:85], v[0:1], v[2:3] op_sel_hi:[0,1,1]
	v_pk_mov_b32 v[4:5], v[84:85], v[122:123] op_sel:[1,0]
	v_mov_b32_e32 v97, v117
	v_pk_fma_f32 v[6:7], v[8:9], v[10:11], v[6:7]
	v_pk_fma_f32 v[0:1], v[4:5], v[34:35], v[2:3]
	v_pk_mul_f32 v[2:3], v[96:97], v[92:93]
	v_mov_b32_dpp v59, v116 row_shl:1 row_mask:0xf bank_mask:0xf
	v_pk_add_f32 v[6:7], v[6:7], 0 op_sel_hi:[1,0]
	v_pk_fma_f32 v[2:3], v[116:117], v[86:87], v[2:3] op_sel_hi:[0,1,1]
	v_pk_mov_b32 v[4:5], v[116:117], v[118:119] op_sel:[1,0]
	v_pk_add_f32 v[0:1], v[6:7], v[0:1]
	v_pk_fma_f32 v[2:3], v[4:5], v[58:59], v[2:3]
	v_mov_b32_e32 v94, v57
	v_pk_add_f32 v[0:1], v[0:1], v[2:3]
	s_mov_b64 s[0:1], 0x1c20000
	v_mov_b32_dpp v94, v115 row_shr:1 row_mask:0xf bank_mask:0xf
	v_mov_b32_e32 v102, v51
	v_mov_b32_e32 v99, v115
	v_lshl_add_u64 v[2:3], v[54:55], 0, s[0:1]
	v_mov_b32_e32 v128, v0
	v_mov_b32_e32 v129, v1
	v_mov_b32_dpp v102, v113 row_shr:1 row_mask:0xf bank_mask:0xf
	v_pk_mul_f32 v[0:1], v[98:99], v[94:95]
	v_mov_b32_e32 v105, v113
	v_mov_b32_dpp v57, v114 row_shl:1 row_mask:0xf bank_mask:0xf
	v_pk_fma_f32 v[0:1], v[114:115], v[124:125], v[0:1] op_sel_hi:[0,1,1]
	v_mov_b32_e32 v14, v115
	v_pk_mul_f32 v[2:3], v[104:105], v[102:103]
	v_mov_b32_dpp v51, v112 row_shl:1 row_mask:0xf bank_mask:0xf
	v_mov_b32_e32 v108, v49
	v_pk_fma_f32 v[0:1], v[14:15], v[56:57], v[0:1]
	v_pk_fma_f32 v[2:3], v[112:113], v[88:89], v[2:3] op_sel_hi:[0,1,1]
	v_mov_b32_e32 v122, v113
	v_mov_b32_dpp v108, v91 row_shr:1 row_mask:0xf bank_mask:0xf
	v_pk_add_f32 v[0:1], v[0:1], 0 op_sel_hi:[1,0]
	v_pk_fma_f32 v[2:3], v[122:123], v[50:51], v[2:3]
	v_mov_b32_e32 v111, v91
	v_pk_add_f32 v[0:1], v[0:1], v[2:3]
	v_pk_mul_f32 v[2:3], v[110:111], v[108:109]
	v_mov_b32_dpp v49, v90 row_shl:1 row_mask:0xf bank_mask:0xf
	v_pk_fma_f32 v[2:3], v[90:91], v[28:29], v[2:3] op_sel_hi:[0,1,1]
	v_mov_b32_e32 v118, v91
	v_pk_fma_f32 v[2:3], v[118:119], v[48:49], v[2:3]
	s_mov_b64 s[0:1], 0x1c30000
	v_pk_add_f32 v[0:1], v[0:1], v[2:3]
	v_lshl_add_u64 v[136:137], v[134:135], 0, s[0:1]
	s_nop 1
	s_mov_b64 vcc, s[28:29]
	s_nop 0
	v_cndmask_b32_dpp v130, v0, v128, vcc quad_perm:[1,0,3,2] row_mask:0xf bank_mask:0xf
	v_cndmask_b32_dpp v131, v1, v129, vcc quad_perm:[1,0,3,2] row_mask:0xf bank_mask:0xf
	s_mov_b64 vcc, s[30:31]
	s_nop 0
	v_cndmask_b32_dpp v132, v128, v0, vcc quad_perm:[1,0,3,2] row_mask:0xf bank_mask:0xf
	v_cndmask_b32_dpp v133, v129, v1, vcc quad_perm:[1,0,3,2] row_mask:0xf bank_mask:0xf
	global_store_dwordx4 v[136:137], v[130:133], off sc0 sc1 nt
	s_nop 1
	s_endpgm

	.amdhsa_kernel _Z7kfinal3PKDF16_PKfS2_S2_PK15HIP_vector_typeIjLj4EES2_Pf
		.amdhsa_group_segment_fixed_size 0
		.amdhsa_private_segment_fixed_size 0
		.amdhsa_kernarg_size 56
		.amdhsa_user_sgpr_count 2
		.amdhsa_user_sgpr_dispatch_ptr 0
		.amdhsa_user_sgpr_queue_ptr 0
		.amdhsa_user_sgpr_kernarg_segment_ptr 1
		.amdhsa_user_sgpr_dispatch_id 0
		.amdhsa_user_sgpr_kernarg_preload_length 0
		.amdhsa_user_sgpr_kernarg_preload_offset 0
		.amdhsa_user_sgpr_private_segment_size 0
		.amdhsa_uses_dynamic_stack 0
		.amdhsa_enable_private_segment 0
		.amdhsa_system_sgpr_workgroup_id_x 1
		.amdhsa_system_sgpr_workgroup_id_y 0
		.amdhsa_system_sgpr_workgroup_id_z 0
		.amdhsa_system_sgpr_workgroup_info 0
		.amdhsa_system_vgpr_workitem_id 0
		.amdhsa_next_free_vgpr 213
		.amdhsa_next_free_sgpr 41
		.amdhsa_accum_offset 140
		.amdhsa_reserve_vcc 1
		.amdhsa_float_round_mode_32 0
		.amdhsa_float_round_mode_16_64 0
		.amdhsa_float_denorm_mode_32 3
		.amdhsa_float_denorm_mode_16_64 3
		.amdhsa_dx10_clamp 1
		.amdhsa_ieee_mode 1
		.amdhsa_fp16_overflow 0
		.amdhsa_tg_split 0
		.amdhsa_exception_fp_ieee_invalid_op 0
		.amdhsa_exception_fp_denorm_src 0
		.amdhsa_exception_fp_ieee_div_zero 0
		.amdhsa_exception_fp_ieee_overflow 0
		.amdhsa_exception_fp_ieee_underflow 0
		.amdhsa_exception_fp_ieee_inexact 0
		.amdhsa_exception_int_div_zero 0
	.end_amdhsa_kernel

amdhsa.kernels:
  - .agpr_count:     0
    .args:
      - .actual_access:  read_only
        .address_space:  global
        .offset:         0
        .size:           8
        .value_kind:     global_buffer
      - .actual_access:  read_only
        .address_space:  global
        .offset:         8
        .size:           8
        .value_kind:     global_buffer
      - .actual_access:  read_only
        .address_space:  global
        .offset:         16
        .size:           8
        .value_kind:     global_buffer
      - .actual_access:  read_only
        .address_space:  global
        .offset:         24
        .size:           8
        .value_kind:     global_buffer
      - .actual_access:  read_only
        .address_space:  global
        .offset:         32
        .size:           8
        .value_kind:     global_buffer
      - .actual_access:  read_only
        .address_space:  global
        .offset:         40
        .size:           8
        .value_kind:     global_buffer
      - .actual_access:  write_only
        .address_space:  global
        .offset:         48
        .size:           8
        .value_kind:     global_buffer
      - .actual_access:  write_only
        .address_space:  global
        .offset:         56
        .size:           8
        .value_kind:     global_buffer
      - .actual_access:  write_only
        .address_space:  global
        .offset:         64
        .size:           8
        .value_kind:     global_buffer
      - .actual_access:  write_only
        .address_space:  global
        .offset:         72
        .size:           8
        .value_kind:     global_buffer
    .group_segment_fixed_size: 12000
    .kernarg_segment_align: 8
    .kernarg_segment_size: 80
    .language:       OpenCL C
    .language_version:
      - 2
      - 0
    .max_flat_workgroup_size: 256
    .name:           _Z2k0PKfS0_S0_S0_S0_S0_PDF16_PfS1_S1_
    .private_segment_fixed_size: 0
    .sgpr_count:     24
    .sgpr_spill_count: 0
    .symbol:         _Z2k0PKfS0_S0_S0_S0_S0_PDF16_PfS1_S1_.kd
    .uniform_work_group_size: 1
    .uses_dynamic_stack: false
    .vgpr_count:     150
    .vgpr_spill_count: 0
    .wavefront_size: 64
  - .agpr_count:     16
    .args:
      - .actual_access:  read_only
        .address_space:  global
        .offset:         0
        .size:           8
        .value_kind:     global_buffer
      - .actual_access:  read_only
        .address_space:  global
        .offset:         8
        .size:           8
        .value_kind:     global_buffer
      - .actual_access:  read_only
        .address_space:  global
        .offset:         16
        .size:           8
        .value_kind:     global_buffer
      - .actual_access:  read_only
        .address_space:  global
        .offset:         24
        .size:           8
        .value_kind:     global_buffer
      - .actual_access:  read_only
        .address_space:  global
        .offset:         32
        .size:           8
        .value_kind:     global_buffer
      - .actual_access:  write_only
        .address_space:  global
        .offset:         40
        .size:           8
        .value_kind:     global_buffer
      - .actual_access:  write_only
        .address_space:  global
        .offset:         48
        .size:           8
        .value_kind:     global_buffer
    .group_segment_fixed_size: 14112
    .kernarg_segment_align: 8
    .kernarg_segment_size: 56
    .language:       OpenCL C
    .language_version:
      - 2
      - 0
    .max_flat_workgroup_size: 256
    .name:           _Z4khidPKDF16_PKfS2_S2_S0_PDF16_Pf
    .private_segment_fixed_size: 0
    .sgpr_count:     24
    .sgpr_spill_count: 0
    .symbol:         _Z4khidPKDF16_PKfS2_S2_S0_PDF16_Pf.kd
    .uniform_work_group_size: 1
    .uses_dynamic_stack: false
    .vgpr_count:     148
    .vgpr_spill_count: 0
    .wavefront_size: 64
  - .agpr_count:     144
    .args:
      - .actual_access:  read_only
        .address_space:  global
        .offset:         0
        .size:           8
        .value_kind:     global_buffer
      - .actual_access:  read_only
        .address_space:  global
        .offset:         8
        .size:           8
        .value_kind:     global_buffer
      - .actual_access:  read_only
        .address_space:  global
        .offset:         16
        .size:           8
        .value_kind:     global_buffer
      - .actual_access:  read_only
        .address_space:  global
        .offset:         24
        .size:           8
        .value_kind:     global_buffer
      - .address_space:  global
        .offset:         32
        .size:           8
        .value_kind:     global_buffer
      - .address_space:  global
        .offset:         40
        .size:           8
        .value_kind:     global_buffer
      - .address_space:  global
        .offset:         48
        .size:           8
        .value_kind:     global_buffer
    .group_segment_fixed_size: 0
    .kernarg_segment_align: 8
    .kernarg_segment_size: 56
    .language:       OpenCL C
    .language_version:
      - 2
      - 0
    .max_flat_workgroup_size: 256
    .name:           _Z6kfinalPKDF16_PKfS2_S2_PK15HIP_vector_typeIjLj4EES2_Pf
    .private_segment_fixed_size: 0
    .sgpr_count:     41
    .sgpr_spill_count: 0
    .symbol:         _Z6kfinalPKDF16_PKfS2_S2_PK15HIP_vector_typeIjLj4EES2_Pf.kd
    .uniform_work_group_size: 1
    .uses_dynamic_stack: false
    .vgpr_count:     400
    .vgpr_spill_count: 0
    .wavefront_size: 64
  - .agpr_count:     73
    .args:
      - .actual_access:  read_only
        .address_space:  global
        .offset:         0
        .size:           8
        .value_kind:     global_buffer
      - .actual_access:  read_only
        .address_space:  global
        .offset:         8
        .size:           8
        .value_kind:     global_buffer
      - .actual_access:  read_only
        .address_space:  global
        .offset:         16
        .size:           8
        .value_kind:     global_buffer
      - .actual_access:  read_only
        .address_space:  global
        .offset:         24
        .size:           8
        .value_kind:     global_buffer
      - .address_space:  global
        .offset:         32
        .size:           8
        .value_kind:     global_buffer
      - .address_space:  global
        .offset:         40
        .size:           8
        .value_kind:     global_buffer
      - .address_space:  global
        .offset:         48
        .size:           8
        .value_kind:     global_buffer
    .group_segment_fixed_size: 0
    .kernarg_segment_align: 8
    .kernarg_segment_size: 56
    .language:       OpenCL C
    .language_version:
      - 2
      - 0
    .max_flat_workgroup_size: 512
    .name:           _Z7kfinal3PKDF16_PKfS2_S2_PK15HIP_vector_typeIjLj4EES2_Pf
    .private_segment_fixed_size: 0
    .sgpr_count:     47
    .sgpr_spill_count: 0
    .symbol:         _Z7kfinal3PKDF16_PKfS2_S2_PK15HIP_vector_typeIjLj4EES2_Pf.kd
    .uniform_work_group_size: 1
    .uses_dynamic_stack: false
    .vgpr_count:     213
    .vgpr_spill_count: 0
    .wavefront_size: 64
